# MLP1 deferred GELU with non-packed VALU ops interleaved ~2.4 per MFMA gap
# speedup vs baseline: 1.0142x; 1.0142x over previous
.Lg_loop:
	s_add_u32 s46, s40, s44
	s_addc_u32 s47, s41, s45
	s_add_u32 s46, s46, 0x180
	s_addc_u32 s47, s47, 0
	s_add_u32 s48, s42, s44
	s_addc_u32 s49, s43, s45
	s_add_u32 s76, s48, 0x180
	s_addc_u32 s77, s49, 0
	s_cmp_eq_u32 s67, s75
	s_cselect_b32 s49, s7, s47
	s_cselect_b32 s48, s6, s46
	s_cselect_b32 s47, s5, s77
	s_cselect_b32 s46, s4, s76
	s_add_i32 s76, s19, s54
	v_lshl_add_u64 v[126:127], v[32:33], 0, s[44:45]
	s_mov_b32 m0, s76
	ds_read_b128 v[44:47], v130 offset:16384
	ds_read_b128 v[56:59], v130 offset:17408
	ds_read_b128 v[60:63], v130 offset:18432
	ds_read_b128 v[64:67], v130 offset:19456
	ds_read_b128 v[68:71], v131
	ds_read_b128 v[96:99], v131 offset:1024
	ds_read_b128 v[136:139], v131 offset:2048
	ds_read_b128 v[140:143], v131 offset:3072
	ds_read_b128 v[144:147], v131 offset:4096
	ds_read_b128 v[148:151], v131 offset:5120
	ds_read_b128 v[152:155], v131 offset:6144
	ds_read_b128 v[156:159], v131 offset:7168
	global_load_lds_dwordx4 v[126:127], off
	v_lshl_add_u64 v[126:127], v[34:35], 0, s[44:45]
	s_add_i32 m0, s76, 0x2000
	s_add_i32 s76, s27, s54
	global_load_lds_dwordx4 v[126:127], off
	v_lshl_add_u64 v[126:127], v[36:37], 0, s[44:45]
	s_mov_b32 m0, s76
	s_nop 0
	global_load_lds_dwordx4 v[126:127], off
	v_lshl_add_u64 v[126:127], v[38:39], 0, s[44:45]
	s_add_i32 m0, s76, 0x2000
	s_nop 0
	global_load_lds_dwordx4 v[126:127], off
	s_barrier
	s_waitcnt lgkmcnt(0)
	s_setprio 1
	s_waitcnt lgkmcnt(0)
	v_mfma_f32_16x16x32_f16 v[92:95], v[44:47], v[68:71], v[92:95]
	v_fma_f32 v242, |v176|, s80, 1.0
	v_fma_f32 v243, |v177|, s80, 1.0
	v_mul_f32_e32 v246, v176, v176
	v_mfma_f32_16x16x32_f16 v[88:91], v[60:63], v[68:71], v[88:91]
	v_rcp_f32_e32 v242, v242
	v_rcp_f32_e32 v243, v243
	v_mfma_f32_16x16x32_f16 v[76:79], v[44:47], v[136:139], v[76:79]
	v_mul_f32_e32 v247, v177, v177
	v_mul_f32_e32 v246, s90, v246
	v_mul_f32_e32 v247, s90, v247
	v_mfma_f32_16x16x32_f16 v[72:75], v[60:63], v[136:139], v[72:75]
	v_fma_f32 v244, v242, s82, v248
	v_fma_f32 v245, v243, s82, v248
	v_mfma_f32_16x16x32_f16 v[28:31], v[44:47], v[144:147], v[28:31]
	v_exp_f32_e32 v246, v246
	v_exp_f32_e32 v247, v247
	v_mfma_f32_16x16x32_f16 v[24:27], v[60:63], v[144:147], v[24:27]
	v_fmaak_f32 v244, v242, v244, 0x3f35f0e3
	v_fmaak_f32 v245, v243, v245, 0x3f35f0e3
	v_fmaak_f32 v244, v242, v244, 0xbe11a98e
	v_mfma_f32_16x16x32_f16 v[12:15], v[44:47], v[152:155], v[12:15]
	v_fmaak_f32 v245, v243, v245, 0xbe11a98e
	v_fmaak_f32 v244, v242, v244, 0x3e027906
	v_mfma_f32_16x16x32_f16 v[8:11], v[60:63], v[152:155], v[8:11]
	v_fmaak_f32 v245, v243, v245, 0x3e027906
	v_mul_f32_e32 v244, v242, v244
	v_mul_f32_e32 v245, v243, v245
	v_mfma_f32_16x16x32_f16 v[92:95], v[56:59], v[96:99], v[92:95]
	v_max_f32_e32 v242, 0, v176
	v_max_f32_e32 v243, 0, v177
	v_mfma_f32_16x16x32_f16 v[88:91], v[64:67], v[96:99], v[88:91]
	v_mul_f32_e32 v244, v244, v246
	v_mul_f32_e32 v245, v245, v247
	v_mfma_f32_16x16x32_f16 v[76:79], v[56:59], v[140:143], v[76:79]
	v_fma_f32 v244, -|v176|, v244, v242
	v_fma_f32 v245, -|v177|, v245, v243
	v_cvt_pk_f16_f32 v176, v244, v245
	v_mfma_f32_16x16x32_f16 v[72:75], v[64:67], v[140:143], v[72:75]
	v_fma_f32 v242, |v178|, s80, 1.0
	v_fma_f32 v243, |v179|, s80, 1.0
	v_mfma_f32_16x16x32_f16 v[28:31], v[56:59], v[148:151], v[28:31]
	v_mul_f32_e32 v246, v178, v178
	v_rcp_f32_e32 v242, v242
	v_rcp_f32_e32 v243, v243
	v_mfma_f32_16x16x32_f16 v[24:27], v[64:67], v[148:151], v[24:27]
	v_mul_f32_e32 v247, v179, v179
	v_mul_f32_e32 v246, s90, v246
	v_mfma_f32_16x16x32_f16 v[12:15], v[56:59], v[156:159], v[12:15]
	v_mul_f32_e32 v247, s90, v247
	v_fma_f32 v244, v242, s82, v248
	v_mfma_f32_16x16x32_f16 v[8:11], v[64:67], v[156:159], v[8:11]
	v_fma_f32 v245, v243, s82, v248
	v_exp_f32_e32 v246, v246
	v_exp_f32_e32 v247, v247
	s_setprio 0
	s_barrier
	s_add_i32 s76, s68, s54
	v_lshl_add_u64 v[126:127], v[40:41], 0, s[44:45]
	s_mov_b32 m0, s76
	ds_read_b128 v[44:47], v130 offset:32768
	ds_read_b128 v[56:59], v130 offset:33792
	ds_read_b128 v[60:63], v130 offset:34816
	ds_read_b128 v[64:67], v130 offset:35840
	global_load_lds_dwordx4 v[126:127], off
	v_lshl_add_u64 v[126:127], v[42:43], 0, s[44:45]
	s_add_i32 m0, s76, 0x2000
	s_nop 0
	global_load_lds_dwordx4 v[126:127], off
	s_waitcnt vmcnt(6)
	s_barrier
	s_waitcnt lgkmcnt(0)
	s_setprio 1
	s_waitcnt lgkmcnt(0)
	v_mfma_f32_16x16x32_f16 v[84:87], v[44:47], v[68:71], v[84:87]
	v_fmaak_f32 v244, v242, v244, 0x3f35f0e3
	v_fmaak_f32 v245, v243, v245, 0x3f35f0e3
	v_mfma_f32_16x16x32_f16 v[52:55], v[44:47], v[136:139], v[52:55]
	v_fmaak_f32 v244, v242, v244, 0xbe11a98e
	v_fmaak_f32 v245, v243, v245, 0xbe11a98e
	v_mfma_f32_16x16x32_f16 v[48:51], v[60:63], v[136:139], v[48:51]
	v_fmaak_f32 v244, v242, v244, 0x3e027906
	v_fmaak_f32 v245, v243, v245, 0x3e027906
	v_mul_f32_e32 v244, v242, v244
	v_mfma_f32_16x16x32_f16 v[20:23], v[44:47], v[144:147], v[20:23]
	v_mul_f32_e32 v245, v243, v245
	v_max_f32_e32 v242, 0, v178
	v_mfma_f32_16x16x32_f16 v[16:19], v[60:63], v[144:147], v[16:19]
	v_max_f32_e32 v243, 0, v179
	v_mul_f32_e32 v244, v244, v246
	v_mul_f32_e32 v245, v245, v247
	v_mfma_f32_16x16x32_f16 v[4:7], v[44:47], v[152:155], v[4:7]
	v_fma_f32 v244, -|v178|, v244, v242
	v_fma_f32 v245, -|v179|, v245, v243
	v_mfma_f32_16x16x32_f16 v[0:3], v[60:63], v[152:155], v[0:3]
	v_cvt_pk_f16_f32 v177, v244, v245
	v_fma_f32 v242, |v180|, s80, 1.0
	v_mfma_f32_16x16x32_f16 v[84:87], v[56:59], v[96:99], v[84:87]
	v_fma_f32 v243, |v181|, s80, 1.0
	v_mul_f32_e32 v246, v180, v180
	v_rcp_f32_e32 v242, v242
	v_mfma_f32_16x16x32_f16 v[68:71], v[60:63], v[68:71], v[80:83]
	v_rcp_f32_e32 v243, v243
	v_mul_f32_e32 v247, v181, v181
	v_mfma_f32_16x16x32_f16 v[52:55], v[56:59], v[140:143], v[52:55]
	v_mul_f32_e32 v246, s90, v246
	v_mul_f32_e32 v247, s90, v247
	v_fma_f32 v244, v242, s82, v248
	v_mfma_f32_16x16x32_f16 v[48:51], v[64:67], v[140:143], v[48:51]
	v_fma_f32 v245, v243, s82, v248
	v_exp_f32_e32 v246, v246
	v_mfma_f32_16x16x32_f16 v[20:23], v[56:59], v[148:151], v[20:23]
	v_exp_f32_e32 v247, v247
	v_fmaak_f32 v244, v242, v244, 0x3f35f0e3
	v_mfma_f32_16x16x32_f16 v[16:19], v[64:67], v[148:151], v[16:19]
	v_fmaak_f32 v245, v243, v245, 0x3f35f0e3
	v_fmaak_f32 v244, v242, v244, 0xbe11a98e
	v_fmaak_f32 v245, v243, v245, 0xbe11a98e
	v_mfma_f32_16x16x32_f16 v[4:7], v[56:59], v[156:159], v[4:7]
	v_fmaak_f32 v244, v242, v244, 0x3e027906
	v_fmaak_f32 v245, v243, v245, 0x3e027906
	v_mfma_f32_16x16x32_f16 v[0:3], v[64:67], v[156:159], v[0:3]
	v_mul_f32_e32 v244, v242, v244
	v_mul_f32_e32 v245, v243, v245
	v_mfma_f32_16x16x32_f16 v[68:71], v[64:67], v[96:99], v[68:71]
	v_max_f32_e32 v242, 0, v180
	v_max_f32_e32 v243, 0, v181
	v_mul_f32_e32 v244, v244, v246
	s_setprio 0
	s_barrier
	s_add_i32 s76, 0, 0x10000
	s_mov_b32 m0, s57
	v_add_u32_e32 v64, s76, v128
	v_lshl_add_u64 v[126:127], s[48:49], 0, v[100:101]
	ds_read_b128 v[44:47], v64
	ds_read_b128 v[56:59], v64 offset:1024
	ds_read_b128 v[60:63], v64 offset:2048
	ds_read_b128 v[64:67], v64 offset:3072
	ds_read_b128 v[80:83], v131 offset:49152
	ds_read_b128 v[96:99], v131 offset:50176
	ds_read_b128 v[136:139], v131 offset:51200
	ds_read_b128 v[140:143], v131 offset:52224
	ds_read_b128 v[144:147], v131 offset:53248
	ds_read_b128 v[148:151], v131 offset:54272
	ds_read_b128 v[152:155], v131 offset:55296
	ds_read_b128 v[156:159], v131 offset:56320
	global_load_lds_dwordx4 v[126:127], off
	v_lshl_add_u64 v[160:161], s[48:49], 0, v[104:105]
	s_mov_b32 m0, s58
	v_lshl_add_u64 v[162:163], s[46:47], 0, v[102:103]
	global_load_lds_dwordx4 v[160:161], off
	s_mov_b32 m0, s59
	v_lshl_add_u64 v[164:165], s[46:47], 0, v[106:107]
	global_load_lds_dwordx4 v[162:163], off
	s_mov_b32 m0, s60
	s_nop 0
	global_load_lds_dwordx4 v[164:165], off
	s_barrier
	s_waitcnt lgkmcnt(0)
	s_setprio 1
	s_waitcnt lgkmcnt(0)
	v_mfma_f32_16x16x32_f16 v[92:95], v[44:47], v[80:83], v[92:95]
	v_mul_f32_e32 v245, v245, v247
	v_fma_f32 v244, -|v180|, v244, v242
	v_mfma_f32_16x16x32_f16 v[88:91], v[60:63], v[80:83], v[88:91]
	v_fma_f32 v245, -|v181|, v245, v243
	v_cvt_pk_f16_f32 v178, v244, v245
	v_fma_f32 v242, |v182|, s80, 1.0
	v_mfma_f32_16x16x32_f16 v[76:79], v[44:47], v[136:139], v[76:79]
	v_fma_f32 v243, |v183|, s80, 1.0
	v_mul_f32_e32 v246, v182, v182
	v_mfma_f32_16x16x32_f16 v[72:75], v[60:63], v[136:139], v[72:75]
	v_rcp_f32_e32 v242, v242
	v_rcp_f32_e32 v243, v243
	v_mfma_f32_16x16x32_f16 v[28:31], v[44:47], v[144:147], v[28:31]
	v_mul_f32_e32 v247, v183, v183
	v_mul_f32_e32 v246, s90, v246
	v_mul_f32_e32 v247, s90, v247
	v_mfma_f32_16x16x32_f16 v[24:27], v[60:63], v[144:147], v[24:27]
	v_fma_f32 v244, v242, s82, v248
	v_fma_f32 v245, v243, s82, v248
	v_mfma_f32_16x16x32_f16 v[12:15], v[44:47], v[152:155], v[12:15]
	v_exp_f32_e32 v246, v246
	v_exp_f32_e32 v247, v247
	v_fmaak_f32 v244, v242, v244, 0x3f35f0e3
	v_mfma_f32_16x16x32_f16 v[8:11], v[60:63], v[152:155], v[8:11]
	v_fmaak_f32 v245, v243, v245, 0x3f35f0e3
	v_fmaak_f32 v244, v242, v244, 0xbe11a98e
	v_mfma_f32_16x16x32_f16 v[92:95], v[56:59], v[96:99], v[92:95]
	v_fmaak_f32 v245, v243, v245, 0xbe11a98e
	v_fmaak_f32 v244, v242, v244, 0x3e027906
	v_mfma_f32_16x16x32_f16 v[88:91], v[64:67], v[96:99], v[88:91]
	v_fmaak_f32 v245, v243, v245, 0x3e027906
	v_mul_f32_e32 v244, v242, v244
	v_mul_f32_e32 v245, v243, v245
	v_mfma_f32_16x16x32_f16 v[76:79], v[56:59], v[140:143], v[76:79]
	v_max_f32_e32 v242, 0, v182
	v_max_f32_e32 v243, 0, v183
	v_mfma_f32_16x16x32_f16 v[72:75], v[64:67], v[140:143], v[72:75]
	v_mul_f32_e32 v244, v244, v246
	v_mul_f32_e32 v245, v245, v247
	v_mfma_f32_16x16x32_f16 v[28:31], v[56:59], v[148:151], v[28:31]
	v_fma_f32 v244, -|v182|, v244, v242
	v_fma_f32 v245, -|v183|, v245, v243
	v_cvt_pk_f16_f32 v179, v244, v245
	v_mfma_f32_16x16x32_f16 v[24:27], v[64:67], v[148:151], v[24:27]
	global_store_dwordx4 v[250:251], v[176:179], off sc1
	v_fma_f32 v242, |v184|, s80, 1.0
	v_mfma_f32_16x16x32_f16 v[12:15], v[56:59], v[156:159], v[12:15]
	v_fma_f32 v243, |v185|, s80, 1.0
	v_mul_f32_e32 v246, v184, v184
	v_rcp_f32_e32 v242, v242
	v_mfma_f32_16x16x32_f16 v[8:11], v[64:67], v[156:159], v[8:11]
	v_rcp_f32_e32 v243, v243
	v_mul_f32_e32 v247, v185, v185
	s_setprio 0
	s_barrier
	s_add_i32 s48, 0, 0x14000
	s_add_u32 s46, s46, s10
	s_addc_u32 s47, s47, s11
	s_mov_b32 m0, s61
	v_add_u32_e32 v64, s48, v128
	v_lshl_add_u64 v[166:167], s[46:47], 0, v[102:103]
	ds_read_b128 v[44:47], v64
	ds_read_b128 v[56:59], v64 offset:1024
	ds_read_b128 v[60:63], v64 offset:2048
	ds_read_b128 v[64:67], v64 offset:3072
	global_load_lds_dwordx4 v[166:167], off
	v_lshl_add_u64 v[168:169], s[46:47], 0, v[106:107]
	s_mov_b32 m0, s62
	s_nop 0
	global_load_lds_dwordx4 v[168:169], off
	s_waitcnt vmcnt(7)
	s_barrier
	s_waitcnt lgkmcnt(0)
	s_setprio 1
	s_waitcnt lgkmcnt(0)
	v_mfma_f32_16x16x32_f16 v[84:87], v[44:47], v[80:83], v[84:87]
	v_mul_f32_e32 v246, s90, v246
	v_mul_f32_e32 v247, s90, v247
	v_mfma_f32_16x16x32_f16 v[52:55], v[44:47], v[136:139], v[52:55]
	v_fma_f32 v244, v242, s82, v248
	v_fma_f32 v245, v243, s82, v248
	v_exp_f32_e32 v246, v246
	v_mfma_f32_16x16x32_f16 v[48:51], v[60:63], v[136:139], v[48:51]
	v_exp_f32_e32 v247, v247
	v_fmaak_f32 v244, v242, v244, 0x3f35f0e3
	v_mfma_f32_16x16x32_f16 v[20:23], v[44:47], v[144:147], v[20:23]
	v_fmaak_f32 v245, v243, v245, 0x3f35f0e3
	v_fmaak_f32 v244, v242, v244, 0xbe11a98e
	v_fmaak_f32 v245, v243, v245, 0xbe11a98e
	v_mfma_f32_16x16x32_f16 v[16:19], v[60:63], v[144:147], v[16:19]
	v_fmaak_f32 v244, v242, v244, 0x3e027906
	v_fmaak_f32 v245, v243, v245, 0x3e027906
	v_mfma_f32_16x16x32_f16 v[4:7], v[44:47], v[152:155], v[4:7]
	v_mul_f32_e32 v244, v242, v244
	v_mul_f32_e32 v245, v243, v245
	v_mfma_f32_16x16x32_f16 v[0:3], v[60:63], v[152:155], v[0:3]
	v_max_f32_e32 v242, 0, v184
	v_max_f32_e32 v243, 0, v185
	v_mul_f32_e32 v244, v244, v246
	v_mfma_f32_16x16x32_f16 v[84:87], v[56:59], v[96:99], v[84:87]
	v_mul_f32_e32 v245, v245, v247
	v_fma_f32 v244, -|v184|, v244, v242
	v_mfma_f32_16x16x32_f16 v[68:71], v[60:63], v[80:83], v[68:71]
	v_fma_f32 v245, -|v185|, v245, v243
	v_cvt_pk_f16_f32 v184, v244, v245
	v_mfma_f32_16x16x32_f16 v[52:55], v[56:59], v[140:143], v[52:55]
	v_fma_f32 v242, |v186|, s80, 1.0
	v_fma_f32 v243, |v187|, s80, 1.0
	v_mul_f32_e32 v246, v186, v186
	v_mfma_f32_16x16x32_f16 v[48:51], v[64:67], v[140:143], v[48:51]
	v_rcp_f32_e32 v242, v242
	v_rcp_f32_e32 v243, v243
	v_mfma_f32_16x16x32_f16 v[20:23], v[56:59], v[148:151], v[20:23]
	v_mul_f32_e32 v247, v187, v187
	v_mul_f32_e32 v246, s90, v246
	v_mul_f32_e32 v247, s90, v247
	v_mfma_f32_16x16x32_f16 v[16:19], v[64:67], v[148:151], v[16:19]
	v_fma_f32 v244, v242, s82, v248
	v_fma_f32 v245, v243, s82, v248
	v_mfma_f32_16x16x32_f16 v[4:7], v[56:59], v[156:159], v[4:7]
	v_exp_f32_e32 v246, v246
	v_exp_f32_e32 v247, v247
	v_mfma_f32_16x16x32_f16 v[0:3], v[64:67], v[156:159], v[0:3]
	v_fmaak_f32 v244, v242, v244, 0x3f35f0e3
	v_fmaak_f32 v245, v243, v245, 0x3f35f0e3
	v_fmaak_f32 v244, v242, v244, 0xbe11a98e
	v_mfma_f32_16x16x32_f16 v[68:71], v[64:67], v[96:99], v[68:71]
	v_fmaak_f32 v245, v243, v245, 0xbe11a98e
	v_fmaak_f32 v244, v242, v244, 0x3e027906
	s_setprio 0
	s_barrier
	s_mov_b32 m0, s64
	v_lshl_add_u64 v[126:127], v[126:127], 0, s[22:23]
	ds_read_b128 v[44:47], v132
	ds_read_b128 v[56:59], v132 offset:1024
	ds_read_b128 v[60:63], v132 offset:2048
	ds_read_b128 v[64:67], v132 offset:3072
	ds_read_b128 v[80:83], v133
	ds_read_b128 v[96:99], v133 offset:1024
	ds_read_b128 v[136:139], v133 offset:2048
	ds_read_b128 v[140:143], v133 offset:3072
	ds_read_b128 v[144:147], v133 offset:4096
	ds_read_b128 v[148:151], v133 offset:5120
	ds_read_b128 v[152:155], v133 offset:6144
	ds_read_b128 v[156:159], v133 offset:7168
	global_load_lds_dwordx4 v[126:127], off
	v_lshl_add_u64 v[126:127], v[160:161], 0, s[22:23]
	s_mov_b32 m0, s65
	s_add_i32 s46, s76, s54
	global_load_lds_dwordx4 v[126:127], off
	v_lshl_add_u64 v[126:127], v[162:163], 0, s[22:23]
	s_mov_b32 m0, s46
	s_nop 0
	global_load_lds_dwordx4 v[126:127], off
	v_lshl_add_u64 v[126:127], v[164:165], 0, s[22:23]
	s_add_i32 m0, s46, 0x2000
	s_nop 0
	global_load_lds_dwordx4 v[126:127], off
	s_barrier
	s_waitcnt lgkmcnt(0)
	s_setprio 1
	s_waitcnt lgkmcnt(0)
	v_mfma_f32_16x16x32_f16 v[92:95], v[44:47], v[80:83], v[92:95]
	v_fmaak_f32 v245, v243, v245, 0x3e027906
	v_mul_f32_e32 v244, v242, v244
	v_mul_f32_e32 v245, v243, v245
	v_mfma_f32_16x16x32_f16 v[88:91], v[60:63], v[80:83], v[88:91]
	v_max_f32_e32 v242, 0, v186
	v_max_f32_e32 v243, 0, v187
	v_mfma_f32_16x16x32_f16 v[76:79], v[44:47], v[136:139], v[76:79]
	v_mul_f32_e32 v244, v244, v246
	v_mul_f32_e32 v245, v245, v247
	v_mfma_f32_16x16x32_f16 v[72:75], v[60:63], v[136:139], v[72:75]
	v_fma_f32 v244, -|v186|, v244, v242
	v_fma_f32 v245, -|v187|, v245, v243
	v_cvt_pk_f16_f32 v185, v244, v245
	v_mfma_f32_16x16x32_f16 v[28:31], v[44:47], v[144:147], v[28:31]
	v_fma_f32 v242, |v188|, s80, 1.0
	v_fma_f32 v243, |v189|, s80, 1.0
	v_mfma_f32_16x16x32_f16 v[24:27], v[60:63], v[144:147], v[24:27]
	v_mul_f32_e32 v246, v188, v188
	v_rcp_f32_e32 v242, v242
	v_rcp_f32_e32 v243, v243
	v_mfma_f32_16x16x32_f16 v[12:15], v[44:47], v[152:155], v[12:15]
	v_mul_f32_e32 v247, v189, v189
	v_mul_f32_e32 v246, s90, v246
	v_mfma_f32_16x16x32_f16 v[8:11], v[60:63], v[152:155], v[8:11]
	v_mul_f32_e32 v247, s90, v247
	v_fma_f32 v244, v242, s82, v248
	v_mfma_f32_16x16x32_f16 v[92:95], v[56:59], v[96:99], v[92:95]
	v_fma_f32 v245, v243, s82, v248
	v_exp_f32_e32 v246, v246
	v_exp_f32_e32 v247, v247
	v_mfma_f32_16x16x32_f16 v[88:91], v[64:67], v[96:99], v[88:91]
	v_fmaak_f32 v244, v242, v244, 0x3f35f0e3
	v_fmaak_f32 v245, v243, v245, 0x3f35f0e3
	v_mfma_f32_16x16x32_f16 v[76:79], v[56:59], v[140:143], v[76:79]
	v_fmaak_f32 v244, v242, v244, 0xbe11a98e
	v_fmaak_f32 v245, v243, v245, 0xbe11a98e
	v_mfma_f32_16x16x32_f16 v[72:75], v[64:67], v[140:143], v[72:75]
	v_fmaak_f32 v244, v242, v244, 0x3e027906
	v_fmaak_f32 v245, v243, v245, 0x3e027906
	v_mul_f32_e32 v244, v242, v244
	v_mfma_f32_16x16x32_f16 v[28:31], v[56:59], v[148:151], v[28:31]
	v_mul_f32_e32 v245, v243, v245
	v_max_f32_e32 v242, 0, v188
	v_mfma_f32_16x16x32_f16 v[24:27], v[64:67], v[148:151], v[24:27]
	v_max_f32_e32 v243, 0, v189
	v_mul_f32_e32 v244, v244, v246
	v_mul_f32_e32 v245, v245, v247
	v_mfma_f32_16x16x32_f16 v[12:15], v[56:59], v[156:159], v[12:15]
	v_fma_f32 v244, -|v188|, v244, v242
	v_fma_f32 v245, -|v189|, v245, v243
	v_mfma_f32_16x16x32_f16 v[8:11], v[64:67], v[156:159], v[8:11]
	v_cvt_pk_f16_f32 v186, v244, v245
	v_fma_f32 v242, |v190|, s80, 1.0
	s_setprio 0
	s_barrier
	s_add_i32 s46, s48, s54
	v_lshl_add_u64 v[126:127], v[166:167], 0, s[22:23]
	s_mov_b32 m0, s46
	ds_read_b128 v[44:47], v134
	ds_read_b128 v[56:59], v134 offset:1024
	ds_read_b128 v[60:63], v134 offset:2048
	ds_read_b128 v[64:67], v134 offset:3072
	global_load_lds_dwordx4 v[126:127], off
	v_lshl_add_u64 v[126:127], v[168:169], 0, s[22:23]
	s_add_i32 m0, s46, 0x2000
	s_nop 0
	global_load_lds_dwordx4 v[126:127], off
	s_waitcnt vmcnt(6)
	s_barrier
	s_waitcnt lgkmcnt(0)
	s_setprio 1
	s_waitcnt lgkmcnt(0)
	v_mfma_f32_16x16x32_f16 v[84:87], v[44:47], v[80:83], v[84:87]
	v_fma_f32 v243, |v191|, s80, 1.0
	v_mul_f32_e32 v246, v190, v190
	v_rcp_f32_e32 v242, v242
	v_mfma_f32_16x16x32_f16 v[68:71], v[60:63], v[80:83], v[68:71]
	v_rcp_f32_e32 v243, v243
	v_mul_f32_e32 v247, v191, v191
	v_mfma_f32_16x16x32_f16 v[52:55], v[44:47], v[136:139], v[52:55]
	v_mul_f32_e32 v246, s90, v246
	v_mul_f32_e32 v247, s90, v247
	v_fma_f32 v244, v242, s82, v248
	v_mfma_f32_16x16x32_f16 v[48:51], v[60:63], v[136:139], v[48:51]
	v_fma_f32 v245, v243, s82, v248
	v_exp_f32_e32 v246, v246
	v_mfma_f32_16x16x32_f16 v[20:23], v[44:47], v[144:147], v[20:23]
	v_exp_f32_e32 v247, v247
	v_fmaak_f32 v244, v242, v244, 0x3f35f0e3
	v_mfma_f32_16x16x32_f16 v[16:19], v[60:63], v[144:147], v[16:19]
	v_fmaak_f32 v245, v243, v245, 0x3f35f0e3
	v_fmaak_f32 v244, v242, v244, 0xbe11a98e
	v_fmaak_f32 v245, v243, v245, 0xbe11a98e
	v_mfma_f32_16x16x32_f16 v[4:7], v[44:47], v[152:155], v[4:7]
	v_fmaak_f32 v244, v242, v244, 0x3e027906
	v_fmaak_f32 v245, v243, v245, 0x3e027906
	v_mfma_f32_16x16x32_f16 v[0:3], v[60:63], v[152:155], v[0:3]
	v_mul_f32_e32 v244, v242, v244
	v_mul_f32_e32 v245, v243, v245
	v_mfma_f32_16x16x32_f16 v[84:87], v[56:59], v[96:99], v[84:87]
	v_max_f32_e32 v242, 0, v190
	v_max_f32_e32 v243, 0, v191
	v_mul_f32_e32 v244, v244, v246
	v_mfma_f32_16x16x32_f16 v[80:83], v[64:67], v[96:99], v[68:71]
	v_mul_f32_e32 v245, v245, v247
	v_fma_f32 v244, -|v190|, v244, v242
	v_mfma_f32_16x16x32_f16 v[52:55], v[56:59], v[140:143], v[52:55]
	v_fma_f32 v245, -|v191|, v245, v243
	v_cvt_pk_f16_f32 v187, v244, v245
	global_store_dwordx4 v[250:251], v[184:187], off offset:256 sc1
	v_mfma_f32_16x16x32_f16 v[48:51], v[64:67], v[140:143], v[48:51]
	v_fma_f32 v242, |v192|, s80, 1.0
	v_fma_f32 v243, |v193|, s80, 1.0
	v_mfma_f32_16x16x32_f16 v[20:23], v[56:59], v[148:151], v[20:23]
	v_mul_f32_e32 v246, v192, v192
	v_rcp_f32_e32 v242, v242
	v_mfma_f32_16x16x32_f16 v[16:19], v[64:67], v[148:151], v[16:19]
	v_rcp_f32_e32 v243, v243
	v_mul_f32_e32 v247, v193, v193
	v_mul_f32_e32 v246, s90, v246
	v_mfma_f32_16x16x32_f16 v[4:7], v[56:59], v[156:159], v[4:7]
	v_mul_f32_e32 v247, s90, v247
	v_fma_f32 v244, v242, s82, v248
	v_mfma_f32_16x16x32_f16 v[0:3], v[64:67], v[156:159], v[0:3]
	v_fma_f32 v245, v243, s82, v248
	v_exp_f32_e32 v246, v246
	v_exp_f32_e32 v247, v247
	s_setprio 0
	s_barrier
	s_add_i32 s75, s75, 3
	s_add_u32 s44, s44, 0x180
	s_addc_u32 s45, s45, 0
	s_add_u32 s46, s40, s44
	s_addc_u32 s47, s41, s45
	s_add_u32 s46, s46, 0x180
	s_addc_u32 s47, s47, 0
	s_add_u32 s48, s42, s44
	s_addc_u32 s49, s43, s45
	s_add_u32 s76, s48, 0x180
	s_addc_u32 s77, s49, 0
	s_cmp_eq_u32 s67, s75
	s_cselect_b32 s49, s7, s47
	s_cselect_b32 s48, s6, s46
	s_cselect_b32 s47, s5, s77
	s_cselect_b32 s46, s4, s76
	s_add_i32 s76, s19, s54
	v_lshl_add_u64 v[126:127], v[32:33], 0, s[44:45]
	s_mov_b32 m0, s76
	ds_read_b128 v[44:47], v130 offset:16384
	ds_read_b128 v[56:59], v130 offset:17408
	ds_read_b128 v[60:63], v130 offset:18432
	ds_read_b128 v[64:67], v130 offset:19456
	ds_read_b128 v[68:71], v131
	ds_read_b128 v[96:99], v131 offset:1024
	ds_read_b128 v[136:139], v131 offset:2048
	ds_read_b128 v[140:143], v131 offset:3072
	ds_read_b128 v[144:147], v131 offset:4096
	ds_read_b128 v[148:151], v131 offset:5120
	ds_read_b128 v[152:155], v131 offset:6144
	ds_read_b128 v[156:159], v131 offset:7168
	global_load_lds_dwordx4 v[126:127], off
	v_lshl_add_u64 v[126:127], v[34:35], 0, s[44:45]
	s_add_i32 m0, s76, 0x2000
	s_add_i32 s76, s27, s54
	global_load_lds_dwordx4 v[126:127], off
	v_lshl_add_u64 v[126:127], v[36:37], 0, s[44:45]
	s_mov_b32 m0, s76
	s_nop 0
	global_load_lds_dwordx4 v[126:127], off
	v_lshl_add_u64 v[126:127], v[38:39], 0, s[44:45]
	s_add_i32 m0, s76, 0x2000
	s_nop 0
	global_load_lds_dwordx4 v[126:127], off
	s_barrier
	s_waitcnt lgkmcnt(0)
	s_setprio 1
	s_waitcnt lgkmcnt(0)
	v_mfma_f32_16x16x32_f16 v[92:95], v[44:47], v[68:71], v[92:95]
	v_fmaak_f32 v244, v242, v244, 0x3f35f0e3
	v_fmaak_f32 v245, v243, v245, 0x3f35f0e3
	v_mfma_f32_16x16x32_f16 v[88:91], v[60:63], v[68:71], v[88:91]
	v_fmaak_f32 v244, v242, v244, 0xbe11a98e
	v_fmaak_f32 v245, v243, v245, 0xbe11a98e
	v_mfma_f32_16x16x32_f16 v[76:79], v[44:47], v[136:139], v[76:79]
	v_fmaak_f32 v244, v242, v244, 0x3e027906
	v_fmaak_f32 v245, v243, v245, 0x3e027906
	v_mul_f32_e32 v244, v242, v244
	v_mfma_f32_16x16x32_f16 v[72:75], v[60:63], v[136:139], v[72:75]
	v_mul_f32_e32 v245, v243, v245
	v_max_f32_e32 v242, 0, v192
	v_mfma_f32_16x16x32_f16 v[28:31], v[44:47], v[144:147], v[28:31]
	v_max_f32_e32 v243, 0, v193
	v_mul_f32_e32 v244, v244, v246
	v_mfma_f32_16x16x32_f16 v[24:27], v[60:63], v[144:147], v[24:27]
	v_mul_f32_e32 v245, v245, v247
	v_fma_f32 v244, -|v192|, v244, v242
	v_fma_f32 v245, -|v193|, v245, v243
	v_mfma_f32_16x16x32_f16 v[12:15], v[44:47], v[152:155], v[12:15]
	v_cvt_pk_f16_f32 v192, v244, v245
	v_fma_f32 v242, |v194|, s80, 1.0
	v_mfma_f32_16x16x32_f16 v[8:11], v[60:63], v[152:155], v[8:11]
	v_fma_f32 v243, |v195|, s80, 1.0
	v_mul_f32_e32 v246, v194, v194
	v_rcp_f32_e32 v242, v242
	v_mfma_f32_16x16x32_f16 v[92:95], v[56:59], v[96:99], v[92:95]
	v_rcp_f32_e32 v243, v243
	v_mul_f32_e32 v247, v195, v195
	v_mfma_f32_16x16x32_f16 v[88:91], v[64:67], v[96:99], v[88:91]
	v_mul_f32_e32 v246, s90, v246
	v_mul_f32_e32 v247, s90, v247
	v_mfma_f32_16x16x32_f16 v[76:79], v[56:59], v[140:143], v[76:79]
	v_fma_f32 v244, v242, s82, v248
	v_fma_f32 v245, v243, s82, v248
	v_exp_f32_e32 v246, v246
	v_mfma_f32_16x16x32_f16 v[72:75], v[64:67], v[140:143], v[72:75]
	v_exp_f32_e32 v247, v247
	v_fmaak_f32 v244, v242, v244, 0x3f35f0e3
	v_mfma_f32_16x16x32_f16 v[28:31], v[56:59], v[148:151], v[28:31]
	v_fmaak_f32 v245, v243, v245, 0x3f35f0e3
	v_fmaak_f32 v244, v242, v244, 0xbe11a98e
	v_fmaak_f32 v245, v243, v245, 0xbe11a98e
	v_mfma_f32_16x16x32_f16 v[24:27], v[64:67], v[148:151], v[24:27]
	v_fmaak_f32 v244, v242, v244, 0x3e027906
	v_fmaak_f32 v245, v243, v245, 0x3e027906
	v_mfma_f32_16x16x32_f16 v[12:15], v[56:59], v[156:159], v[12:15]
	v_mul_f32_e32 v244, v242, v244
	v_mul_f32_e32 v245, v243, v245
	v_mfma_f32_16x16x32_f16 v[8:11], v[64:67], v[156:159], v[8:11]
	v_max_f32_e32 v242, 0, v194
	v_max_f32_e32 v243, 0, v195
	v_mul_f32_e32 v244, v244, v246
	s_setprio 0
	s_barrier
	s_add_i32 s76, s68, s54
	v_lshl_add_u64 v[126:127], v[40:41], 0, s[44:45]
	s_mov_b32 m0, s76
	ds_read_b128 v[44:47], v130 offset:32768
	ds_read_b128 v[56:59], v130 offset:33792
	ds_read_b128 v[60:63], v130 offset:34816
	ds_read_b128 v[64:67], v130 offset:35840
	global_load_lds_dwordx4 v[126:127], off
	v_lshl_add_u64 v[126:127], v[42:43], 0, s[44:45]
	s_add_i32 m0, s76, 0x2000
	s_nop 0
	global_load_lds_dwordx4 v[126:127], off
	s_waitcnt vmcnt(7)
	s_barrier
	s_waitcnt lgkmcnt(0)
	s_setprio 1
	s_waitcnt lgkmcnt(0)
	v_mfma_f32_16x16x32_f16 v[84:87], v[44:47], v[68:71], v[84:87]
	v_mul_f32_e32 v245, v245, v247
	v_fma_f32 v244, -|v194|, v244, v242
	v_mfma_f32_16x16x32_f16 v[52:55], v[44:47], v[136:139], v[52:55]
	v_fma_f32 v245, -|v195|, v245, v243
	v_cvt_pk_f16_f32 v193, v244, v245
	v_mfma_f32_16x16x32_f16 v[48:51], v[60:63], v[136:139], v[48:51]
	v_fma_f32 v242, |v196|, s80, 1.0
	v_fma_f32 v243, |v197|, s80, 1.0
	v_mul_f32_e32 v246, v196, v196
	v_mfma_f32_16x16x32_f16 v[20:23], v[44:47], v[144:147], v[20:23]
	v_rcp_f32_e32 v242, v242
	v_rcp_f32_e32 v243, v243
	v_mfma_f32_16x16x32_f16 v[16:19], v[60:63], v[144:147], v[16:19]
	v_mul_f32_e32 v247, v197, v197
	v_mul_f32_e32 v246, s90, v246
	v_mul_f32_e32 v247, s90, v247
	v_mfma_f32_16x16x32_f16 v[4:7], v[44:47], v[152:155], v[4:7]
	v_fma_f32 v244, v242, s82, v248
	v_fma_f32 v245, v243, s82, v248
	v_mfma_f32_16x16x32_f16 v[0:3], v[60:63], v[152:155], v[0:3]
	v_exp_f32_e32 v246, v246
	v_exp_f32_e32 v247, v247
	v_mfma_f32_16x16x32_f16 v[84:87], v[56:59], v[96:99], v[84:87]
	v_fmaak_f32 v244, v242, v244, 0x3f35f0e3
	v_fmaak_f32 v245, v243, v245, 0x3f35f0e3
	v_fmaak_f32 v244, v242, v244, 0xbe11a98e
	v_mfma_f32_16x16x32_f16 v[68:71], v[60:63], v[68:71], v[80:83]
	v_fmaak_f32 v245, v243, v245, 0xbe11a98e
	v_fmaak_f32 v244, v242, v244, 0x3e027906
	v_mfma_f32_16x16x32_f16 v[52:55], v[56:59], v[140:143], v[52:55]
	v_fmaak_f32 v245, v243, v245, 0x3e027906
	v_mul_f32_e32 v244, v242, v244
	v_mul_f32_e32 v245, v243, v245
	v_mfma_f32_16x16x32_f16 v[48:51], v[64:67], v[140:143], v[48:51]
	v_max_f32_e32 v242, 0, v196
	v_max_f32_e32 v243, 0, v197
	v_mfma_f32_16x16x32_f16 v[20:23], v[56:59], v[148:151], v[20:23]
	v_mul_f32_e32 v244, v244, v246
	v_mul_f32_e32 v245, v245, v247
	v_mfma_f32_16x16x32_f16 v[16:19], v[64:67], v[148:151], v[16:19]
	v_fma_f32 v244, -|v196|, v244, v242
	v_fma_f32 v245, -|v197|, v245, v243
	v_cvt_pk_f16_f32 v194, v244, v245
	v_mfma_f32_16x16x32_f16 v[4:7], v[56:59], v[156:159], v[4:7]
	v_fma_f32 v242, |v198|, s80, 1.0
	v_fma_f32 v243, |v199|, s80, 1.0
	v_mfma_f32_16x16x32_f16 v[0:3], v[64:67], v[156:159], v[0:3]
	v_mul_f32_e32 v246, v198, v198
	v_rcp_f32_e32 v242, v242
	v_rcp_f32_e32 v243, v243
	v_mfma_f32_16x16x32_f16 v[68:71], v[64:67], v[96:99], v[68:71]
	v_mul_f32_e32 v247, v199, v199
	v_mul_f32_e32 v246, s90, v246
	s_setprio 0
	s_barrier
	s_add_i32 s76, 0, 0x10000
	s_mov_b32 m0, s57
	v_add_u32_e32 v64, s76, v128
	v_lshl_add_u64 v[126:127], s[48:49], 0, v[100:101]
	ds_read_b128 v[44:47], v64
	ds_read_b128 v[56:59], v64 offset:1024
	ds_read_b128 v[60:63], v64 offset:2048
	ds_read_b128 v[64:67], v64 offset:3072
	ds_read_b128 v[80:83], v131 offset:49152
	ds_read_b128 v[96:99], v131 offset:50176
	ds_read_b128 v[136:139], v131 offset:51200
	ds_read_b128 v[140:143], v131 offset:52224
	ds_read_b128 v[144:147], v131 offset:53248
	ds_read_b128 v[148:151], v131 offset:54272
	ds_read_b128 v[152:155], v131 offset:55296
	ds_read_b128 v[156:159], v131 offset:56320
	global_load_lds_dwordx4 v[126:127], off
	v_lshl_add_u64 v[160:161], s[48:49], 0, v[104:105]
	s_mov_b32 m0, s58
	v_lshl_add_u64 v[162:163], s[46:47], 0, v[102:103]
	global_load_lds_dwordx4 v[160:161], off
	s_mov_b32 m0, s59
	v_lshl_add_u64 v[164:165], s[46:47], 0, v[106:107]
	global_load_lds_dwordx4 v[162:163], off
	s_mov_b32 m0, s60
	s_nop 0
	global_load_lds_dwordx4 v[164:165], off
	s_barrier
	s_waitcnt lgkmcnt(0)
	s_setprio 1
	s_waitcnt lgkmcnt(0)
	v_mfma_f32_16x16x32_f16 v[92:95], v[44:47], v[80:83], v[92:95]
	v_mul_f32_e32 v247, s90, v247
	v_fma_f32 v244, v242, s82, v248
	v_mfma_f32_16x16x32_f16 v[88:91], v[60:63], v[80:83], v[88:91]
	v_fma_f32 v245, v243, s82, v248
	v_exp_f32_e32 v246, v246
	v_exp_f32_e32 v247, v247
	v_mfma_f32_16x16x32_f16 v[76:79], v[44:47], v[136:139], v[76:79]
	v_fmaak_f32 v244, v242, v244, 0x3f35f0e3
	v_fmaak_f32 v245, v243, v245, 0x3f35f0e3
	v_mfma_f32_16x16x32_f16 v[72:75], v[60:63], v[136:139], v[72:75]
	v_fmaak_f32 v244, v242, v244, 0xbe11a98e
	v_fmaak_f32 v245, v243, v245, 0xbe11a98e
	v_mfma_f32_16x16x32_f16 v[28:31], v[44:47], v[144:147], v[28:31]
	v_fmaak_f32 v244, v242, v244, 0x3e027906
	v_fmaak_f32 v245, v243, v245, 0x3e027906
	v_mul_f32_e32 v244, v242, v244
	v_mfma_f32_16x16x32_f16 v[24:27], v[60:63], v[144:147], v[24:27]
	v_mul_f32_e32 v245, v243, v245
	v_max_f32_e32 v242, 0, v198
	v_mfma_f32_16x16x32_f16 v[12:15], v[44:47], v[152:155], v[12:15]
	v_max_f32_e32 v243, 0, v199
	v_mul_f32_e32 v244, v244, v246
	v_mul_f32_e32 v245, v245, v247
	v_mfma_f32_16x16x32_f16 v[8:11], v[60:63], v[152:155], v[8:11]
	v_fma_f32 v244, -|v198|, v244, v242
	v_fma_f32 v245, -|v199|, v245, v243
	v_mfma_f32_16x16x32_f16 v[92:95], v[56:59], v[96:99], v[92:95]
	v_cvt_pk_f16_f32 v195, v244, v245
	v_lshl_add_u64 v[252:253], v[250:251], 0, s[92:93]
	v_mfma_f32_16x16x32_f16 v[88:91], v[64:67], v[96:99], v[88:91]
	global_store_dwordx4 v[252:253], v[192:195], off sc1
	v_fma_f32 v242, |v200|, s80, 1.0
	v_fma_f32 v243, |v201|, s80, 1.0
	v_mfma_f32_16x16x32_f16 v[76:79], v[56:59], v[140:143], v[76:79]
	v_mul_f32_e32 v246, v200, v200
	v_rcp_f32_e32 v242, v242
	v_mfma_f32_16x16x32_f16 v[72:75], v[64:67], v[140:143], v[72:75]
	v_rcp_f32_e32 v243, v243
	v_mul_f32_e32 v247, v201, v201
	v_mul_f32_e32 v246, s90, v246
	v_mfma_f32_16x16x32_f16 v[28:31], v[56:59], v[148:151], v[28:31]
	v_mul_f32_e32 v247, s90, v247
	v_fma_f32 v244, v242, s82, v248
	v_mfma_f32_16x16x32_f16 v[24:27], v[64:67], v[148:151], v[24:27]
	v_fma_f32 v245, v243, s82, v248
	v_exp_f32_e32 v246, v246
	v_mfma_f32_16x16x32_f16 v[12:15], v[56:59], v[156:159], v[12:15]
	v_exp_f32_e32 v247, v247
	v_fmaak_f32 v244, v242, v244, 0x3f35f0e3
	v_fmaak_f32 v245, v243, v245, 0x3f35f0e3
	v_mfma_f32_16x16x32_f16 v[8:11], v[64:67], v[156:159], v[8:11]
	v_fmaak_f32 v244, v242, v244, 0xbe11a98e
	v_fmaak_f32 v245, v243, v245, 0xbe11a98e
	s_setprio 0
	s_barrier
	s_add_i32 s48, 0, 0x14000
	s_add_u32 s46, s46, s10
	s_addc_u32 s47, s47, s11
	s_mov_b32 m0, s61
	v_add_u32_e32 v64, s48, v128
	v_lshl_add_u64 v[166:167], s[46:47], 0, v[102:103]
	ds_read_b128 v[44:47], v64
	ds_read_b128 v[56:59], v64 offset:1024
	ds_read_b128 v[60:63], v64 offset:2048
	ds_read_b128 v[64:67], v64 offset:3072
	global_load_lds_dwordx4 v[166:167], off
	v_lshl_add_u64 v[168:169], s[46:47], 0, v[106:107]
	s_mov_b32 m0, s62
	s_nop 0
	global_load_lds_dwordx4 v[168:169], off
	s_waitcnt vmcnt(7)
	s_barrier
	s_waitcnt lgkmcnt(0)
	s_setprio 1
	s_waitcnt lgkmcnt(0)
	v_mfma_f32_16x16x32_f16 v[84:87], v[44:47], v[80:83], v[84:87]
	v_fmaak_f32 v244, v242, v244, 0x3e027906
	v_fmaak_f32 v245, v243, v245, 0x3e027906
	v_mfma_f32_16x16x32_f16 v[52:55], v[44:47], v[136:139], v[52:55]
	v_mul_f32_e32 v244, v242, v244
	v_mul_f32_e32 v245, v243, v245
	v_max_f32_e32 v242, 0, v200
	v_mfma_f32_16x16x32_f16 v[48:51], v[60:63], v[136:139], v[48:51]
	v_max_f32_e32 v243, 0, v201
	v_mul_f32_e32 v244, v244, v246
	v_mfma_f32_16x16x32_f16 v[20:23], v[44:47], v[144:147], v[20:23]
	v_mul_f32_e32 v245, v245, v247
	v_fma_f32 v244, -|v200|, v244, v242
	v_fma_f32 v245, -|v201|, v245, v243
	v_mfma_f32_16x16x32_f16 v[16:19], v[60:63], v[144:147], v[16:19]
	v_cvt_pk_f16_f32 v200, v244, v245
	v_fma_f32 v242, |v202|, s80, 1.0
	v_mfma_f32_16x16x32_f16 v[4:7], v[44:47], v[152:155], v[4:7]
	v_fma_f32 v243, |v203|, s80, 1.0
	v_mul_f32_e32 v246, v202, v202
	v_mfma_f32_16x16x32_f16 v[0:3], v[60:63], v[152:155], v[0:3]
	v_rcp_f32_e32 v242, v242
	v_rcp_f32_e32 v243, v243
	v_mul_f32_e32 v247, v203, v203
	v_mfma_f32_16x16x32_f16 v[84:87], v[56:59], v[96:99], v[84:87]
	v_mul_f32_e32 v246, s90, v246
	v_mul_f32_e32 v247, s90, v247
	v_mfma_f32_16x16x32_f16 v[68:71], v[60:63], v[80:83], v[68:71]
	v_fma_f32 v244, v242, s82, v248
	v_fma_f32 v245, v243, s82, v248
	v_exp_f32_e32 v246, v246
	v_mfma_f32_16x16x32_f16 v[52:55], v[56:59], v[140:143], v[52:55]
	v_exp_f32_e32 v247, v247
	v_fmaak_f32 v244, v242, v244, 0x3f35f0e3
	v_mfma_f32_16x16x32_f16 v[48:51], v[64:67], v[140:143], v[48:51]
	v_fmaak_f32 v245, v243, v245, 0x3f35f0e3
	v_fmaak_f32 v244, v242, v244, 0xbe11a98e
	v_mfma_f32_16x16x32_f16 v[20:23], v[56:59], v[148:151], v[20:23]
	v_fmaak_f32 v245, v243, v245, 0xbe11a98e
	v_fmaak_f32 v244, v242, v244, 0x3e027906
	v_fmaak_f32 v245, v243, v245, 0x3e027906
	v_mfma_f32_16x16x32_f16 v[16:19], v[64:67], v[148:151], v[16:19]
	v_mul_f32_e32 v244, v242, v244
	v_mul_f32_e32 v245, v243, v245
	v_mfma_f32_16x16x32_f16 v[4:7], v[56:59], v[156:159], v[4:7]
	v_max_f32_e32 v242, 0, v202
	v_max_f32_e32 v243, 0, v203
	v_mfma_f32_16x16x32_f16 v[0:3], v[64:67], v[156:159], v[0:3]
	v_mul_f32_e32 v244, v244, v246
	v_mul_f32_e32 v245, v245, v247
	v_fma_f32 v244, -|v202|, v244, v242
	v_mfma_f32_16x16x32_f16 v[68:71], v[64:67], v[96:99], v[68:71]
	v_fma_f32 v245, -|v203|, v245, v243
	v_cvt_pk_f16_f32 v201, v244, v245
	s_setprio 0
	s_barrier
	s_mov_b32 m0, s64
	v_lshl_add_u64 v[126:127], v[126:127], 0, s[22:23]
	ds_read_b128 v[44:47], v132
	ds_read_b128 v[56:59], v132 offset:1024
	ds_read_b128 v[60:63], v132 offset:2048
	ds_read_b128 v[64:67], v132 offset:3072
	ds_read_b128 v[80:83], v133
	ds_read_b128 v[96:99], v133 offset:1024
	ds_read_b128 v[136:139], v133 offset:2048
	ds_read_b128 v[140:143], v133 offset:3072
	ds_read_b128 v[144:147], v133 offset:4096
	ds_read_b128 v[148:151], v133 offset:5120
	ds_read_b128 v[152:155], v133 offset:6144
	ds_read_b128 v[156:159], v133 offset:7168
	global_load_lds_dwordx4 v[126:127], off
	v_lshl_add_u64 v[126:127], v[160:161], 0, s[22:23]
	s_mov_b32 m0, s65
	s_add_i32 s46, s76, s54
	global_load_lds_dwordx4 v[126:127], off
	v_lshl_add_u64 v[126:127], v[162:163], 0, s[22:23]
	s_mov_b32 m0, s46
	s_nop 0
	global_load_lds_dwordx4 v[126:127], off
	v_lshl_add_u64 v[126:127], v[164:165], 0, s[22:23]
	s_add_i32 m0, s46, 0x2000
	s_nop 0
	global_load_lds_dwordx4 v[126:127], off
	s_barrier
	s_waitcnt lgkmcnt(0)
	s_setprio 1
	s_waitcnt lgkmcnt(0)
	v_mfma_f32_16x16x32_f16 v[92:95], v[44:47], v[80:83], v[92:95]
	v_fma_f32 v242, |v204|, s80, 1.0
	v_fma_f32 v243, |v205|, s80, 1.0
	v_mul_f32_e32 v246, v204, v204
	v_mfma_f32_16x16x32_f16 v[88:91], v[60:63], v[80:83], v[88:91]
	v_rcp_f32_e32 v242, v242
	v_rcp_f32_e32 v243, v243
	v_mfma_f32_16x16x32_f16 v[76:79], v[44:47], v[136:139], v[76:79]
	v_mul_f32_e32 v247, v205, v205
	v_mul_f32_e32 v246, s90, v246
	v_mfma_f32_16x16x32_f16 v[72:75], v[60:63], v[136:139], v[72:75]
	v_mul_f32_e32 v247, s90, v247
	v_fma_f32 v244, v242, s82, v248
	v_fma_f32 v245, v243, s82, v248
	v_mfma_f32_16x16x32_f16 v[28:31], v[44:47], v[144:147], v[28:31]
	v_exp_f32_e32 v246, v246
	v_exp_f32_e32 v247, v247
	v_mfma_f32_16x16x32_f16 v[24:27], v[60:63], v[144:147], v[24:27]
	v_fmaak_f32 v244, v242, v244, 0x3f35f0e3
	v_fmaak_f32 v245, v243, v245, 0x3f35f0e3
	v_fmaak_f32 v244, v242, v244, 0xbe11a98e
	v_mfma_f32_16x16x32_f16 v[12:15], v[44:47], v[152:155], v[12:15]
	v_fmaak_f32 v245, v243, v245, 0xbe11a98e
	v_fmaak_f32 v244, v242, v244, 0x3e027906
	v_mfma_f32_16x16x32_f16 v[8:11], v[60:63], v[152:155], v[8:11]
	v_fmaak_f32 v245, v243, v245, 0x3e027906
	v_mul_f32_e32 v244, v242, v244
	v_mfma_f32_16x16x32_f16 v[92:95], v[56:59], v[96:99], v[92:95]
	v_mul_f32_e32 v245, v243, v245
	v_max_f32_e32 v242, 0, v204
	v_max_f32_e32 v243, 0, v205
	v_mfma_f32_16x16x32_f16 v[88:91], v[64:67], v[96:99], v[88:91]
	v_mul_f32_e32 v244, v244, v246
	v_mul_f32_e32 v245, v245, v247
	v_mfma_f32_16x16x32_f16 v[76:79], v[56:59], v[140:143], v[76:79]
	v_fma_f32 v244, -|v204|, v244, v242
	v_fma_f32 v245, -|v205|, v245, v243
	v_mfma_f32_16x16x32_f16 v[72:75], v[64:67], v[140:143], v[72:75]
	v_cvt_pk_f16_f32 v202, v244, v245
	v_fma_f32 v242, |v206|, s80, 1.0
	v_fma_f32 v243, |v207|, s80, 1.0
	v_mfma_f32_16x16x32_f16 v[28:31], v[56:59], v[148:151], v[28:31]
	v_mul_f32_e32 v246, v206, v206
	v_rcp_f32_e32 v242, v242
	v_mfma_f32_16x16x32_f16 v[24:27], v[64:67], v[148:151], v[24:27]
	v_rcp_f32_e32 v243, v243
	v_mul_f32_e32 v247, v207, v207
	v_mul_f32_e32 v246, s90, v246
	v_mfma_f32_16x16x32_f16 v[12:15], v[56:59], v[156:159], v[12:15]
	v_mul_f32_e32 v247, s90, v247
	v_fma_f32 v244, v242, s82, v248
	v_mfma_f32_16x16x32_f16 v[8:11], v[64:67], v[156:159], v[8:11]
	v_fma_f32 v245, v243, s82, v248
	v_exp_f32_e32 v246, v246
	s_setprio 0
	s_barrier
	s_add_i32 s46, s48, s54
	v_lshl_add_u64 v[126:127], v[166:167], 0, s[22:23]
	s_mov_b32 m0, s46
	ds_read_b128 v[44:47], v134
	ds_read_b128 v[56:59], v134 offset:1024
	ds_read_b128 v[60:63], v134 offset:2048
	ds_read_b128 v[64:67], v134 offset:3072
	global_load_lds_dwordx4 v[126:127], off
	v_lshl_add_u64 v[126:127], v[168:169], 0, s[22:23]
	s_add_i32 m0, s46, 0x2000
	s_nop 0
	global_load_lds_dwordx4 v[126:127], off
	s_waitcnt vmcnt(6)
	s_barrier
	s_waitcnt lgkmcnt(0)
	s_setprio 1
	s_waitcnt lgkmcnt(0)
	v_mfma_f32_16x16x32_f16 v[84:87], v[44:47], v[80:83], v[84:87]
	v_exp_f32_e32 v247, v247
	v_fmaak_f32 v244, v242, v244, 0x3f35f0e3
	v_fmaak_f32 v245, v243, v245, 0x3f35f0e3
	v_mfma_f32_16x16x32_f16 v[68:71], v[60:63], v[80:83], v[68:71]
	v_fmaak_f32 v244, v242, v244, 0xbe11a98e
	v_fmaak_f32 v245, v243, v245, 0xbe11a98e
	v_mfma_f32_16x16x32_f16 v[52:55], v[44:47], v[136:139], v[52:55]
	v_fmaak_f32 v244, v242, v244, 0x3e027906
	v_fmaak_f32 v245, v243, v245, 0x3e027906
	v_mul_f32_e32 v244, v242, v244
	v_mfma_f32_16x16x32_f16 v[48:51], v[60:63], v[136:139], v[48:51]
	v_mul_f32_e32 v245, v243, v245
	v_max_f32_e32 v242, 0, v206
	v_mfma_f32_16x16x32_f16 v[20:23], v[44:47], v[144:147], v[20:23]
	v_max_f32_e32 v243, 0, v207
	v_mul_f32_e32 v244, v244, v246
	v_mfma_f32_16x16x32_f16 v[16:19], v[60:63], v[144:147], v[16:19]
	v_mul_f32_e32 v245, v245, v247
	v_fma_f32 v244, -|v206|, v244, v242
	v_fma_f32 v245, -|v207|, v245, v243
	v_mfma_f32_16x16x32_f16 v[4:7], v[44:47], v[152:155], v[4:7]
	v_cvt_pk_f16_f32 v203, v244, v245
	v_lshl_add_u64 v[252:253], v[250:251], 0, s[92:93]
	v_mfma_f32_16x16x32_f16 v[0:3], v[60:63], v[152:155], v[0:3]
	global_store_dwordx4 v[252:253], v[200:203], off offset:256 sc1
	v_fma_f32 v242, |v208|, s80, 1.0
	v_mfma_f32_16x16x32_f16 v[84:87], v[56:59], v[96:99], v[84:87]
	v_fma_f32 v243, |v209|, s80, 1.0
	v_mul_f32_e32 v246, v208, v208
	v_rcp_f32_e32 v242, v242
	v_mfma_f32_16x16x32_f16 v[80:83], v[64:67], v[96:99], v[68:71]
	v_rcp_f32_e32 v243, v243
	v_mul_f32_e32 v247, v209, v209
	v_mfma_f32_16x16x32_f16 v[52:55], v[56:59], v[140:143], v[52:55]
	v_mul_f32_e32 v246, s90, v246
	v_mul_f32_e32 v247, s90, v247
	v_fma_f32 v244, v242, s82, v248
	v_mfma_f32_16x16x32_f16 v[48:51], v[64:67], v[140:143], v[48:51]
	v_fma_f32 v245, v243, s82, v248
	v_exp_f32_e32 v246, v246
	v_mfma_f32_16x16x32_f16 v[20:23], v[56:59], v[148:151], v[20:23]
	v_exp_f32_e32 v247, v247
	v_fmaak_f32 v244, v242, v244, 0x3f35f0e3
	v_mfma_f32_16x16x32_f16 v[16:19], v[64:67], v[148:151], v[16:19]
	v_fmaak_f32 v245, v243, v245, 0x3f35f0e3
	v_fmaak_f32 v244, v242, v244, 0xbe11a98e
	v_fmaak_f32 v245, v243, v245, 0xbe11a98e
	v_mfma_f32_16x16x32_f16 v[4:7], v[56:59], v[156:159], v[4:7]
	v_fmaak_f32 v244, v242, v244, 0x3e027906
	v_fmaak_f32 v245, v243, v245, 0x3e027906
	v_mfma_f32_16x16x32_f16 v[0:3], v[64:67], v[156:159], v[0:3]
	v_mul_f32_e32 v244, v242, v244
	v_mul_f32_e32 v245, v243, v245
	v_max_f32_e32 v242, 0, v208
	s_setprio 0
	s_barrier
	s_add_i32 s75, s75, 3
	s_add_u32 s44, s44, 0x180
	s_addc_u32 s45, s45, 0
	s_add_u32 s46, s40, s44
	s_addc_u32 s47, s41, s45
	s_add_u32 s46, s46, 0x180
	s_addc_u32 s47, s47, 0
	s_add_u32 s48, s42, s44
	s_addc_u32 s49, s43, s45
	s_add_u32 s76, s48, 0x180
	s_addc_u32 s77, s49, 0
	s_cmp_eq_u32 s67, s75
	s_cselect_b32 s49, s7, s47
	s_cselect_b32 s48, s6, s46
	s_cselect_b32 s47, s5, s77
	s_cselect_b32 s46, s4, s76
	s_add_i32 s76, s19, s54
	v_lshl_add_u64 v[126:127], v[32:33], 0, s[44:45]
	s_mov_b32 m0, s76
	ds_read_b128 v[44:47], v130 offset:16384
	ds_read_b128 v[56:59], v130 offset:17408
	ds_read_b128 v[60:63], v130 offset:18432
	ds_read_b128 v[64:67], v130 offset:19456
	ds_read_b128 v[68:71], v131
	ds_read_b128 v[96:99], v131 offset:1024
	ds_read_b128 v[136:139], v131 offset:2048
	ds_read_b128 v[140:143], v131 offset:3072
	ds_read_b128 v[144:147], v131 offset:4096
	ds_read_b128 v[148:151], v131 offset:5120
	ds_read_b128 v[152:155], v131 offset:6144
	ds_read_b128 v[156:159], v131 offset:7168
	global_load_lds_dwordx4 v[126:127], off
	v_lshl_add_u64 v[126:127], v[34:35], 0, s[44:45]
	s_add_i32 m0, s76, 0x2000
	s_add_i32 s76, s27, s54
	global_load_lds_dwordx4 v[126:127], off
	v_lshl_add_u64 v[126:127], v[36:37], 0, s[44:45]
	s_mov_b32 m0, s76
	s_nop 0
	global_load_lds_dwordx4 v[126:127], off
	v_lshl_add_u64 v[126:127], v[38:39], 0, s[44:45]
	s_add_i32 m0, s76, 0x2000
	s_nop 0
	global_load_lds_dwordx4 v[126:127], off
	s_barrier
	s_waitcnt lgkmcnt(0)
	s_setprio 1
	s_waitcnt lgkmcnt(0)
	v_mfma_f32_16x16x32_f16 v[92:95], v[44:47], v[68:71], v[92:95]
	v_max_f32_e32 v243, 0, v209
	v_mul_f32_e32 v244, v244, v246
	v_mfma_f32_16x16x32_f16 v[88:91], v[60:63], v[68:71], v[88:91]
	v_mul_f32_e32 v245, v245, v247
	v_fma_f32 v244, -|v208|, v244, v242
	v_mfma_f32_16x16x32_f16 v[76:79], v[44:47], v[136:139], v[76:79]
	v_fma_f32 v245, -|v209|, v245, v243
	v_cvt_pk_f16_f32 v208, v244, v245
	v_fma_f32 v242, |v210|, s80, 1.0
	v_mfma_f32_16x16x32_f16 v[72:75], v[60:63], v[136:139], v[72:75]
	v_fma_f32 v243, |v211|, s80, 1.0
	v_mul_f32_e32 v246, v210, v210
	v_mfma_f32_16x16x32_f16 v[28:31], v[44:47], v[144:147], v[28:31]
	v_rcp_f32_e32 v242, v242
	v_rcp_f32_e32 v243, v243
	v_mul_f32_e32 v247, v211, v211
	v_mfma_f32_16x16x32_f16 v[24:27], v[60:63], v[144:147], v[24:27]
	v_mul_f32_e32 v246, s90, v246
	v_mul_f32_e32 v247, s90, v247
	v_mfma_f32_16x16x32_f16 v[12:15], v[44:47], v[152:155], v[12:15]
	v_fma_f32 v244, v242, s82, v248
	v_fma_f32 v245, v243, s82, v248
	v_mfma_f32_16x16x32_f16 v[8:11], v[60:63], v[152:155], v[8:11]
	v_exp_f32_e32 v246, v246
	v_exp_f32_e32 v247, v247
	v_fmaak_f32 v244, v242, v244, 0x3f35f0e3
	v_mfma_f32_16x16x32_f16 v[92:95], v[56:59], v[96:99], v[92:95]
	v_fmaak_f32 v245, v243, v245, 0x3f35f0e3
	v_fmaak_f32 v244, v242, v244, 0xbe11a98e
	v_mfma_f32_16x16x32_f16 v[88:91], v[64:67], v[96:99], v[88:91]
	v_fmaak_f32 v245, v243, v245, 0xbe11a98e
	v_fmaak_f32 v244, v242, v244, 0x3e027906
	v_mfma_f32_16x16x32_f16 v[76:79], v[56:59], v[140:143], v[76:79]
	v_fmaak_f32 v245, v243, v245, 0x3e027906
	v_mul_f32_e32 v244, v242, v244
	v_mul_f32_e32 v245, v243, v245
	v_mfma_f32_16x16x32_f16 v[72:75], v[64:67], v[140:143], v[72:75]
	v_max_f32_e32 v242, 0, v210
	v_max_f32_e32 v243, 0, v211
	v_mfma_f32_16x16x32_f16 v[28:31], v[56:59], v[148:151], v[28:31]
	v_mul_f32_e32 v244, v244, v246
	v_mul_f32_e32 v245, v245, v247
	v_fma_f32 v244, -|v210|, v244, v242
	v_mfma_f32_16x16x32_f16 v[24:27], v[64:67], v[148:151], v[24:27]
	v_fma_f32 v245, -|v211|, v245, v243
	v_cvt_pk_f16_f32 v209, v244, v245
	v_mfma_f32_16x16x32_f16 v[12:15], v[56:59], v[156:159], v[12:15]
	v_fma_f32 v242, |v212|, s80, 1.0
	v_fma_f32 v243, |v213|, s80, 1.0
	v_mfma_f32_16x16x32_f16 v[8:11], v[64:67], v[156:159], v[8:11]
	v_mul_f32_e32 v246, v212, v212
	v_rcp_f32_e32 v242, v242
	v_rcp_f32_e32 v243, v243
	s_setprio 0
	s_barrier
	s_add_i32 s76, s68, s54
	v_lshl_add_u64 v[126:127], v[40:41], 0, s[44:45]
	s_mov_b32 m0, s76
	ds_read_b128 v[44:47], v130 offset:32768
	ds_read_b128 v[56:59], v130 offset:33792
	ds_read_b128 v[60:63], v130 offset:34816
	ds_read_b128 v[64:67], v130 offset:35840
	global_load_lds_dwordx4 v[126:127], off
	v_lshl_add_u64 v[126:127], v[42:43], 0, s[44:45]
	s_add_i32 m0, s76, 0x2000
	s_nop 0
	global_load_lds_dwordx4 v[126:127], off
	s_waitcnt vmcnt(7)
	s_barrier
	s_waitcnt lgkmcnt(0)
	s_setprio 1
	s_waitcnt lgkmcnt(0)
	v_mfma_f32_16x16x32_f16 v[84:87], v[44:47], v[68:71], v[84:87]
	v_mul_f32_e32 v247, v213, v213
	v_mul_f32_e32 v246, s90, v246
	v_mfma_f32_16x16x32_f16 v[52:55], v[44:47], v[136:139], v[52:55]
	v_mul_f32_e32 v247, s90, v247
	v_fma_f32 v244, v242, s82, v248
	v_fma_f32 v245, v243, s82, v248
	v_mfma_f32_16x16x32_f16 v[48:51], v[60:63], v[136:139], v[48:51]
	v_exp_f32_e32 v246, v246
	v_exp_f32_e32 v247, v247
	v_mfma_f32_16x16x32_f16 v[20:23], v[44:47], v[144:147], v[20:23]
	v_fmaak_f32 v244, v242, v244, 0x3f35f0e3
	v_fmaak_f32 v245, v243, v245, 0x3f35f0e3
	v_mfma_f32_16x16x32_f16 v[16:19], v[60:63], v[144:147], v[16:19]
	v_fmaak_f32 v244, v242, v244, 0xbe11a98e
	v_fmaak_f32 v245, v243, v245, 0xbe11a98e
	v_fmaak_f32 v244, v242, v244, 0x3e027906
	v_mfma_f32_16x16x32_f16 v[4:7], v[44:47], v[152:155], v[4:7]
	v_fmaak_f32 v245, v243, v245, 0x3e027906
	v_mul_f32_e32 v244, v242, v244
	v_mfma_f32_16x16x32_f16 v[0:3], v[60:63], v[152:155], v[0:3]
	v_mul_f32_e32 v245, v243, v245
	v_max_f32_e32 v242, 0, v212
	v_mfma_f32_16x16x32_f16 v[84:87], v[56:59], v[96:99], v[84:87]
	v_max_f32_e32 v243, 0, v213
	v_mul_f32_e32 v244, v244, v246
	v_mul_f32_e32 v245, v245, v247
	v_mfma_f32_16x16x32_f16 v[68:71], v[60:63], v[68:71], v[80:83]
	v_fma_f32 v244, -|v212|, v244, v242
	v_fma_f32 v245, -|v213|, v245, v243
	v_mfma_f32_16x16x32_f16 v[52:55], v[56:59], v[140:143], v[52:55]
	v_cvt_pk_f16_f32 v210, v244, v245
	v_fma_f32 v242, |v214|, s80, 1.0
	v_fma_f32 v243, |v215|, s80, 1.0
	v_mfma_f32_16x16x32_f16 v[48:51], v[64:67], v[140:143], v[48:51]
	v_mul_f32_e32 v246, v214, v214
	v_rcp_f32_e32 v242, v242
	v_mfma_f32_16x16x32_f16 v[20:23], v[56:59], v[148:151], v[20:23]
	v_rcp_f32_e32 v243, v243
	v_mul_f32_e32 v247, v215, v215
	v_mfma_f32_16x16x32_f16 v[16:19], v[64:67], v[148:151], v[16:19]
	v_mul_f32_e32 v246, s90, v246
	v_mul_f32_e32 v247, s90, v247
	v_fma_f32 v244, v242, s82, v248
	v_mfma_f32_16x16x32_f16 v[4:7], v[56:59], v[156:159], v[4:7]
	v_fma_f32 v245, v243, s82, v248
	v_exp_f32_e32 v246, v246
	v_mfma_f32_16x16x32_f16 v[0:3], v[64:67], v[156:159], v[0:3]
	v_exp_f32_e32 v247, v247
	v_fmaak_f32 v244, v242, v244, 0x3f35f0e3
	v_fmaak_f32 v245, v243, v245, 0x3f35f0e3
	v_mfma_f32_16x16x32_f16 v[68:71], v[64:67], v[96:99], v[68:71]
	v_fmaak_f32 v244, v242, v244, 0xbe11a98e
	v_fmaak_f32 v245, v243, v245, 0xbe11a98e
	s_setprio 0
	s_barrier
	s_add_i32 s76, 0, 0x10000
	s_mov_b32 m0, s57
	v_add_u32_e32 v64, s76, v128
	v_lshl_add_u64 v[126:127], s[48:49], 0, v[100:101]
	ds_read_b128 v[44:47], v64
	ds_read_b128 v[56:59], v64 offset:1024
	ds_read_b128 v[60:63], v64 offset:2048
	ds_read_b128 v[64:67], v64 offset:3072
	ds_read_b128 v[80:83], v131 offset:49152
	ds_read_b128 v[96:99], v131 offset:50176
	ds_read_b128 v[136:139], v131 offset:51200
	ds_read_b128 v[140:143], v131 offset:52224
	ds_read_b128 v[144:147], v131 offset:53248
	ds_read_b128 v[148:151], v131 offset:54272
	ds_read_b128 v[152:155], v131 offset:55296
	ds_read_b128 v[156:159], v131 offset:56320
	global_load_lds_dwordx4 v[126:127], off
	v_lshl_add_u64 v[160:161], s[48:49], 0, v[104:105]
	s_mov_b32 m0, s58
	v_lshl_add_u64 v[162:163], s[46:47], 0, v[102:103]
	global_load_lds_dwordx4 v[160:161], off
	s_mov_b32 m0, s59
	v_lshl_add_u64 v[164:165], s[46:47], 0, v[106:107]
	global_load_lds_dwordx4 v[162:163], off
	s_mov_b32 m0, s60
	s_nop 0
	global_load_lds_dwordx4 v[164:165], off
	s_barrier
	s_waitcnt lgkmcnt(0)
	s_setprio 1
	s_waitcnt lgkmcnt(0)
	v_mfma_f32_16x16x32_f16 v[92:95], v[44:47], v[80:83], v[92:95]
	v_fmaak_f32 v244, v242, v244, 0x3e027906
	v_fmaak_f32 v245, v243, v245, 0x3e027906
	v_mfma_f32_16x16x32_f16 v[88:91], v[60:63], v[80:83], v[88:91]
	v_mul_f32_e32 v244, v242, v244
	v_mul_f32_e32 v245, v243, v245
	v_max_f32_e32 v242, 0, v214
	v_mfma_f32_16x16x32_f16 v[76:79], v[44:47], v[136:139], v[76:79]
	v_max_f32_e32 v243, 0, v215
	v_mul_f32_e32 v244, v244, v246
	v_mfma_f32_16x16x32_f16 v[72:75], v[60:63], v[136:139], v[72:75]
	v_mul_f32_e32 v245, v245, v247
	v_fma_f32 v244, -|v214|, v244, v242
	v_mfma_f32_16x16x32_f16 v[28:31], v[44:47], v[144:147], v[28:31]
	v_fma_f32 v245, -|v215|, v245, v243
	v_cvt_pk_f16_f32 v211, v244, v245
	v_lshl_add_u64 v[252:253], v[250:251], 0, s[94:95]
	v_mfma_f32_16x16x32_f16 v[24:27], v[60:63], v[144:147], v[24:27]
	global_store_dwordx4 v[252:253], v[208:211], off sc1
	v_fma_f32 v242, |v216|, s80, 1.0
	v_mfma_f32_16x16x32_f16 v[12:15], v[44:47], v[152:155], v[12:15]
	v_fma_f32 v243, |v217|, s80, 1.0
	v_mul_f32_e32 v246, v216, v216
	v_rcp_f32_e32 v242, v242
	v_mfma_f32_16x16x32_f16 v[8:11], v[60:63], v[152:155], v[8:11]
	v_rcp_f32_e32 v243, v243
	v_mul_f32_e32 v247, v217, v217
	v_mfma_f32_16x16x32_f16 v[92:95], v[56:59], v[96:99], v[92:95]
	v_mul_f32_e32 v246, s90, v246
	v_mul_f32_e32 v247, s90, v247
	v_mfma_f32_16x16x32_f16 v[88:91], v[64:67], v[96:99], v[88:91]
	v_fma_f32 v244, v242, s82, v248
	v_fma_f32 v245, v243, s82, v248
	v_exp_f32_e32 v246, v246
	v_mfma_f32_16x16x32_f16 v[76:79], v[56:59], v[140:143], v[76:79]
	v_exp_f32_e32 v247, v247
	v_fmaak_f32 v244, v242, v244, 0x3f35f0e3
	v_mfma_f32_16x16x32_f16 v[72:75], v[64:67], v[140:143], v[72:75]
	v_fmaak_f32 v245, v243, v245, 0x3f35f0e3
	v_fmaak_f32 v244, v242, v244, 0xbe11a98e
	v_fmaak_f32 v245, v243, v245, 0xbe11a98e
	v_mfma_f32_16x16x32_f16 v[28:31], v[56:59], v[148:151], v[28:31]
	v_fmaak_f32 v244, v242, v244, 0x3e027906
	v_fmaak_f32 v245, v243, v245, 0x3e027906
	v_mfma_f32_16x16x32_f16 v[24:27], v[64:67], v[148:151], v[24:27]
	v_mul_f32_e32 v244, v242, v244
	v_mul_f32_e32 v245, v243, v245
	v_mfma_f32_16x16x32_f16 v[12:15], v[56:59], v[156:159], v[12:15]
	v_max_f32_e32 v242, 0, v216
	v_max_f32_e32 v243, 0, v217
	v_mul_f32_e32 v244, v244, v246
	v_mfma_f32_16x16x32_f16 v[8:11], v[64:67], v[156:159], v[8:11]
	v_mul_f32_e32 v245, v245, v247
	v_fma_f32 v244, -|v216|, v244, v242
	s_setprio 0
	s_barrier
	s_add_i32 s48, 0, 0x14000
	s_add_u32 s46, s46, s10
	s_addc_u32 s47, s47, s11
	s_mov_b32 m0, s61
	v_add_u32_e32 v64, s48, v128
	v_lshl_add_u64 v[166:167], s[46:47], 0, v[102:103]
	ds_read_b128 v[44:47], v64
	ds_read_b128 v[56:59], v64 offset:1024
	ds_read_b128 v[60:63], v64 offset:2048
	ds_read_b128 v[64:67], v64 offset:3072
	global_load_lds_dwordx4 v[166:167], off
	v_lshl_add_u64 v[168:169], s[46:47], 0, v[106:107]
	s_mov_b32 m0, s62
	s_nop 0
	global_load_lds_dwordx4 v[168:169], off
	s_waitcnt vmcnt(7)
	s_barrier
	s_waitcnt lgkmcnt(0)
	s_setprio 1
	s_waitcnt lgkmcnt(0)
	v_mfma_f32_16x16x32_f16 v[84:87], v[44:47], v[80:83], v[84:87]
	v_fma_f32 v245, -|v217|, v245, v243
	v_cvt_pk_f16_f32 v216, v244, v245
	v_mfma_f32_16x16x32_f16 v[52:55], v[44:47], v[136:139], v[52:55]
	v_fma_f32 v242, |v218|, s80, 1.0
	v_fma_f32 v243, |v219|, s80, 1.0
	v_mul_f32_e32 v246, v218, v218
	v_mfma_f32_16x16x32_f16 v[48:51], v[60:63], v[136:139], v[48:51]
	v_rcp_f32_e32 v242, v242
	v_rcp_f32_e32 v243, v243
	v_mfma_f32_16x16x32_f16 v[20:23], v[44:47], v[144:147], v[20:23]
	v_mul_f32_e32 v247, v219, v219
	v_mul_f32_e32 v246, s90, v246
	v_mul_f32_e32 v247, s90, v247
	v_mfma_f32_16x16x32_f16 v[16:19], v[60:63], v[144:147], v[16:19]
	v_fma_f32 v244, v242, s82, v248
	v_fma_f32 v245, v243, s82, v248
	v_mfma_f32_16x16x32_f16 v[4:7], v[44:47], v[152:155], v[4:7]
	v_exp_f32_e32 v246, v246
	v_exp_f32_e32 v247, v247
	v_mfma_f32_16x16x32_f16 v[0:3], v[60:63], v[152:155], v[0:3]
	v_fmaak_f32 v244, v242, v244, 0x3f35f0e3
	v_fmaak_f32 v245, v243, v245, 0x3f35f0e3
	v_fmaak_f32 v244, v242, v244, 0xbe11a98e
	v_mfma_f32_16x16x32_f16 v[84:87], v[56:59], v[96:99], v[84:87]
	v_fmaak_f32 v245, v243, v245, 0xbe11a98e
	v_fmaak_f32 v244, v242, v244, 0x3e027906
	v_mfma_f32_16x16x32_f16 v[68:71], v[60:63], v[80:83], v[68:71]
	v_fmaak_f32 v245, v243, v245, 0x3e027906
	v_mul_f32_e32 v244, v242, v244
	v_mul_f32_e32 v245, v243, v245
	v_mfma_f32_16x16x32_f16 v[52:55], v[56:59], v[140:143], v[52:55]
	v_max_f32_e32 v242, 0, v218
	v_max_f32_e32 v243, 0, v219
	v_mfma_f32_16x16x32_f16 v[48:51], v[64:67], v[140:143], v[48:51]
	v_mul_f32_e32 v244, v244, v246
	v_mul_f32_e32 v245, v245, v247
	v_mfma_f32_16x16x32_f16 v[20:23], v[56:59], v[148:151], v[20:23]
	v_fma_f32 v244, -|v218|, v244, v242
	v_fma_f32 v245, -|v219|, v245, v243
	v_cvt_pk_f16_f32 v217, v244, v245
	v_mfma_f32_16x16x32_f16 v[16:19], v[64:67], v[148:151], v[16:19]
	v_fma_f32 v242, |v220|, s80, 1.0
	v_fma_f32 v243, |v221|, s80, 1.0
	v_mfma_f32_16x16x32_f16 v[4:7], v[56:59], v[156:159], v[4:7]
	v_mul_f32_e32 v246, v220, v220
	v_rcp_f32_e32 v242, v242
	v_rcp_f32_e32 v243, v243
	v_mfma_f32_16x16x32_f16 v[0:3], v[64:67], v[156:159], v[0:3]
	v_mul_f32_e32 v247, v221, v221
	v_mul_f32_e32 v246, s90, v246
	v_mfma_f32_16x16x32_f16 v[68:71], v[64:67], v[96:99], v[68:71]
	v_mul_f32_e32 v247, s90, v247
	v_fma_f32 v244, v242, s82, v248
	s_setprio 0
	s_barrier
	s_mov_b32 m0, s64
	v_lshl_add_u64 v[126:127], v[126:127], 0, s[22:23]
	ds_read_b128 v[44:47], v132
	ds_read_b128 v[56:59], v132 offset:1024
	ds_read_b128 v[60:63], v132 offset:2048
	ds_read_b128 v[64:67], v132 offset:3072
	ds_read_b128 v[80:83], v133
	ds_read_b128 v[96:99], v133 offset:1024
	ds_read_b128 v[136:139], v133 offset:2048
	ds_read_b128 v[140:143], v133 offset:3072
	ds_read_b128 v[144:147], v133 offset:4096
	ds_read_b128 v[148:151], v133 offset:5120
	ds_read_b128 v[152:155], v133 offset:6144
	ds_read_b128 v[156:159], v133 offset:7168
	global_load_lds_dwordx4 v[126:127], off
	v_lshl_add_u64 v[126:127], v[160:161], 0, s[22:23]
	s_mov_b32 m0, s65
	s_add_i32 s46, s76, s54
	global_load_lds_dwordx4 v[126:127], off
	v_lshl_add_u64 v[126:127], v[162:163], 0, s[22:23]
	s_mov_b32 m0, s46
	s_nop 0
	global_load_lds_dwordx4 v[126:127], off
	v_lshl_add_u64 v[126:127], v[164:165], 0, s[22:23]
	s_add_i32 m0, s46, 0x2000
	s_nop 0
	global_load_lds_dwordx4 v[126:127], off
	s_barrier
	s_waitcnt lgkmcnt(0)
	s_setprio 1
	s_waitcnt lgkmcnt(0)
	v_mfma_f32_16x16x32_f16 v[92:95], v[44:47], v[80:83], v[92:95]
	v_fma_f32 v245, v243, s82, v248
	v_exp_f32_e32 v246, v246
	v_exp_f32_e32 v247, v247
	v_mfma_f32_16x16x32_f16 v[88:91], v[60:63], v[80:83], v[88:91]
	v_fmaak_f32 v244, v242, v244, 0x3f35f0e3
	v_fmaak_f32 v245, v243, v245, 0x3f35f0e3
	v_mfma_f32_16x16x32_f16 v[76:79], v[44:47], v[136:139], v[76:79]
	v_fmaak_f32 v244, v242, v244, 0xbe11a98e
	v_fmaak_f32 v245, v243, v245, 0xbe11a98e
	v_mfma_f32_16x16x32_f16 v[72:75], v[60:63], v[136:139], v[72:75]
	v_fmaak_f32 v244, v242, v244, 0x3e027906
	v_fmaak_f32 v245, v243, v245, 0x3e027906
	v_mul_f32_e32 v244, v242, v244
	v_mfma_f32_16x16x32_f16 v[28:31], v[44:47], v[144:147], v[28:31]
	v_mul_f32_e32 v245, v243, v245
	v_max_f32_e32 v242, 0, v220
	v_mfma_f32_16x16x32_f16 v[24:27], v[60:63], v[144:147], v[24:27]
	v_max_f32_e32 v243, 0, v221
	v_mul_f32_e32 v244, v244, v246
	v_mul_f32_e32 v245, v245, v247
	v_mfma_f32_16x16x32_f16 v[12:15], v[44:47], v[152:155], v[12:15]
	v_fma_f32 v244, -|v220|, v244, v242
	v_fma_f32 v245, -|v221|, v245, v243
	v_mfma_f32_16x16x32_f16 v[8:11], v[60:63], v[152:155], v[8:11]
	v_cvt_pk_f16_f32 v218, v244, v245
	v_fma_f32 v242, |v222|, s80, 1.0
	v_mfma_f32_16x16x32_f16 v[92:95], v[56:59], v[96:99], v[92:95]
	v_fma_f32 v243, |v223|, s80, 1.0
	v_mul_f32_e32 v246, v222, v222
	v_rcp_f32_e32 v242, v242
	v_mfma_f32_16x16x32_f16 v[88:91], v[64:67], v[96:99], v[88:91]
	v_rcp_f32_e32 v243, v243
	v_mul_f32_e32 v247, v223, v223
	v_mfma_f32_16x16x32_f16 v[76:79], v[56:59], v[140:143], v[76:79]
	v_mul_f32_e32 v246, s90, v246
	v_mul_f32_e32 v247, s90, v247
	v_fma_f32 v244, v242, s82, v248
	v_mfma_f32_16x16x32_f16 v[72:75], v[64:67], v[140:143], v[72:75]
	v_fma_f32 v245, v243, s82, v248
	v_exp_f32_e32 v246, v246
	v_mfma_f32_16x16x32_f16 v[28:31], v[56:59], v[148:151], v[28:31]
	v_exp_f32_e32 v247, v247
	v_fmaak_f32 v244, v242, v244, 0x3f35f0e3
	v_mfma_f32_16x16x32_f16 v[24:27], v[64:67], v[148:151], v[24:27]
	v_fmaak_f32 v245, v243, v245, 0x3f35f0e3
	v_fmaak_f32 v244, v242, v244, 0xbe11a98e
	v_fmaak_f32 v245, v243, v245, 0xbe11a98e
	v_mfma_f32_16x16x32_f16 v[12:15], v[56:59], v[156:159], v[12:15]
	v_fmaak_f32 v244, v242, v244, 0x3e027906
	v_fmaak_f32 v245, v243, v245, 0x3e027906
	v_mfma_f32_16x16x32_f16 v[8:11], v[64:67], v[156:159], v[8:11]
	v_mul_f32_e32 v244, v242, v244
	v_mul_f32_e32 v245, v243, v245
	s_setprio 0
	s_barrier
	s_add_i32 s46, s48, s54
	v_lshl_add_u64 v[126:127], v[166:167], 0, s[22:23]
	s_mov_b32 m0, s46
	ds_read_b128 v[44:47], v134
	ds_read_b128 v[56:59], v134 offset:1024
	ds_read_b128 v[60:63], v134 offset:2048
	ds_read_b128 v[64:67], v134 offset:3072
	global_load_lds_dwordx4 v[126:127], off
	v_lshl_add_u64 v[126:127], v[168:169], 0, s[22:23]
	s_add_i32 m0, s46, 0x2000
	s_nop 0
	global_load_lds_dwordx4 v[126:127], off
	s_waitcnt vmcnt(6)
	s_barrier
	s_waitcnt lgkmcnt(0)
	s_setprio 1
	s_waitcnt lgkmcnt(0)
	v_mfma_f32_16x16x32_f16 v[84:87], v[44:47], v[80:83], v[84:87]
	v_max_f32_e32 v242, 0, v222
	v_max_f32_e32 v243, 0, v223
	v_mul_f32_e32 v244, v244, v246
	v_mfma_f32_16x16x32_f16 v[68:71], v[60:63], v[80:83], v[68:71]
	v_mul_f32_e32 v245, v245, v247
	v_fma_f32 v244, -|v222|, v244, v242
	v_mfma_f32_16x16x32_f16 v[52:55], v[44:47], v[136:139], v[52:55]
	v_fma_f32 v245, -|v223|, v245, v243
	v_cvt_pk_f16_f32 v219, v244, v245
	v_lshl_add_u64 v[252:253], v[250:251], 0, s[94:95]
	v_mfma_f32_16x16x32_f16 v[48:51], v[60:63], v[136:139], v[48:51]
	global_store_dwordx4 v[252:253], v[216:219], off offset:256 sc1
	v_fma_f32 v242, |v224|, s80, 1.0
	v_mfma_f32_16x16x32_f16 v[20:23], v[44:47], v[144:147], v[20:23]
	v_fma_f32 v243, |v225|, s80, 1.0
	v_mul_f32_e32 v246, v224, v224
	v_mfma_f32_16x16x32_f16 v[16:19], v[60:63], v[144:147], v[16:19]
	v_rcp_f32_e32 v242, v242
	v_rcp_f32_e32 v243, v243
	v_mul_f32_e32 v247, v225, v225
	v_mfma_f32_16x16x32_f16 v[4:7], v[44:47], v[152:155], v[4:7]
	v_mul_f32_e32 v246, s90, v246
	v_mul_f32_e32 v247, s90, v247
	v_mfma_f32_16x16x32_f16 v[0:3], v[60:63], v[152:155], v[0:3]
	v_fma_f32 v244, v242, s82, v248
	v_fma_f32 v245, v243, s82, v248
	v_exp_f32_e32 v246, v246
	v_mfma_f32_16x16x32_f16 v[84:87], v[56:59], v[96:99], v[84:87]
	v_exp_f32_e32 v247, v247
	v_fmaak_f32 v244, v242, v244, 0x3f35f0e3
	v_mfma_f32_16x16x32_f16 v[80:83], v[64:67], v[96:99], v[68:71]
	v_fmaak_f32 v245, v243, v245, 0x3f35f0e3
	v_fmaak_f32 v244, v242, v244, 0xbe11a98e
	v_mfma_f32_16x16x32_f16 v[52:55], v[56:59], v[140:143], v[52:55]
	v_fmaak_f32 v245, v243, v245, 0xbe11a98e
	v_fmaak_f32 v244, v242, v244, 0x3e027906
	v_fmaak_f32 v245, v243, v245, 0x3e027906
	v_mfma_f32_16x16x32_f16 v[48:51], v[64:67], v[140:143], v[48:51]
	v_mul_f32_e32 v244, v242, v244
	v_mul_f32_e32 v245, v243, v245
	v_mfma_f32_16x16x32_f16 v[20:23], v[56:59], v[148:151], v[20:23]
	v_max_f32_e32 v242, 0, v224
	v_max_f32_e32 v243, 0, v225
	v_mfma_f32_16x16x32_f16 v[16:19], v[64:67], v[148:151], v[16:19]
	v_mul_f32_e32 v244, v244, v246
	v_mul_f32_e32 v245, v245, v247
	v_fma_f32 v244, -|v224|, v244, v242
	v_mfma_f32_16x16x32_f16 v[4:7], v[56:59], v[156:159], v[4:7]
	v_fma_f32 v245, -|v225|, v245, v243
	v_cvt_pk_f16_f32 v224, v244, v245
	v_mfma_f32_16x16x32_f16 v[0:3], v[64:67], v[156:159], v[0:3]
	v_fma_f32 v242, |v226|, s80, 1.0
	v_fma_f32 v243, |v227|, s80, 1.0
	v_mul_f32_e32 v246, v226, v226
	s_setprio 0
	s_barrier
	s_add_i32 s75, s75, 3
	s_add_u32 s44, s44, 0x180
	s_addc_u32 s45, s45, 0
	s_add_u32 s46, s40, s44
	s_addc_u32 s47, s41, s45
	s_add_u32 s46, s46, 0x180
	s_addc_u32 s47, s47, 0
	s_add_u32 s48, s42, s44
	s_addc_u32 s49, s43, s45
	s_add_u32 s76, s48, 0x180
	s_addc_u32 s77, s49, 0
	s_cmp_eq_u32 s67, s75
	s_cselect_b32 s49, s7, s47
	s_cselect_b32 s48, s6, s46
	s_cselect_b32 s47, s5, s77
	s_cselect_b32 s46, s4, s76
	s_add_i32 s76, s19, s54
	v_lshl_add_u64 v[126:127], v[32:33], 0, s[44:45]
	s_mov_b32 m0, s76
	ds_read_b128 v[44:47], v130 offset:16384
	ds_read_b128 v[56:59], v130 offset:17408
	ds_read_b128 v[60:63], v130 offset:18432
	ds_read_b128 v[64:67], v130 offset:19456
	ds_read_b128 v[68:71], v131
	ds_read_b128 v[96:99], v131 offset:1024
	ds_read_b128 v[136:139], v131 offset:2048
	ds_read_b128 v[140:143], v131 offset:3072
	ds_read_b128 v[144:147], v131 offset:4096
	ds_read_b128 v[148:151], v131 offset:5120
	ds_read_b128 v[152:155], v131 offset:6144
	ds_read_b128 v[156:159], v131 offset:7168
	global_load_lds_dwordx4 v[126:127], off
	v_lshl_add_u64 v[126:127], v[34:35], 0, s[44:45]
	s_add_i32 m0, s76, 0x2000
	s_add_i32 s76, s27, s54
	global_load_lds_dwordx4 v[126:127], off
	v_lshl_add_u64 v[126:127], v[36:37], 0, s[44:45]
	s_mov_b32 m0, s76
	s_nop 0
	global_load_lds_dwordx4 v[126:127], off
	v_lshl_add_u64 v[126:127], v[38:39], 0, s[44:45]
	s_add_i32 m0, s76, 0x2000
	s_nop 0
	global_load_lds_dwordx4 v[126:127], off
	s_barrier
	s_waitcnt lgkmcnt(0)
	s_setprio 1
	s_waitcnt lgkmcnt(0)
	v_mfma_f32_16x16x32_f16 v[92:95], v[44:47], v[68:71], v[92:95]
	v_rcp_f32_e32 v242, v242
	v_rcp_f32_e32 v243, v243
	v_mfma_f32_16x16x32_f16 v[88:91], v[60:63], v[68:71], v[88:91]
	v_mul_f32_e32 v247, v227, v227
	v_mul_f32_e32 v246, s90, v246
	v_mfma_f32_16x16x32_f16 v[76:79], v[44:47], v[136:139], v[76:79]
	v_mul_f32_e32 v247, s90, v247
	v_fma_f32 v244, v242, s82, v248
	v_fma_f32 v245, v243, s82, v248
	v_mfma_f32_16x16x32_f16 v[72:75], v[60:63], v[136:139], v[72:75]
	v_exp_f32_e32 v246, v246
	v_exp_f32_e32 v247, v247
	v_mfma_f32_16x16x32_f16 v[28:31], v[44:47], v[144:147], v[28:31]
	v_fmaak_f32 v244, v242, v244, 0x3f35f0e3
	v_fmaak_f32 v245, v243, v245, 0x3f35f0e3
	v_fmaak_f32 v244, v242, v244, 0xbe11a98e
	v_mfma_f32_16x16x32_f16 v[24:27], v[60:63], v[144:147], v[24:27]
	v_fmaak_f32 v245, v243, v245, 0xbe11a98e
	v_fmaak_f32 v244, v242, v244, 0x3e027906
	v_mfma_f32_16x16x32_f16 v[12:15], v[44:47], v[152:155], v[12:15]
	v_fmaak_f32 v245, v243, v245, 0x3e027906
	v_mul_f32_e32 v244, v242, v244
	v_mfma_f32_16x16x32_f16 v[8:11], v[60:63], v[152:155], v[8:11]
	v_mul_f32_e32 v245, v243, v245
	v_max_f32_e32 v242, 0, v226
	v_max_f32_e32 v243, 0, v227
	v_mfma_f32_16x16x32_f16 v[92:95], v[56:59], v[96:99], v[92:95]
	v_mul_f32_e32 v244, v244, v246
	v_mul_f32_e32 v245, v245, v247
	v_mfma_f32_16x16x32_f16 v[88:91], v[64:67], v[96:99], v[88:91]
	v_fma_f32 v244, -|v226|, v244, v242
	v_fma_f32 v245, -|v227|, v245, v243
	v_mfma_f32_16x16x32_f16 v[76:79], v[56:59], v[140:143], v[76:79]
	v_cvt_pk_f16_f32 v225, v244, v245
	v_fma_f32 v242, |v228|, s80, 1.0
	v_fma_f32 v243, |v229|, s80, 1.0
	v_mfma_f32_16x16x32_f16 v[72:75], v[64:67], v[140:143], v[72:75]
	v_mul_f32_e32 v246, v228, v228
	v_rcp_f32_e32 v242, v242
	v_mfma_f32_16x16x32_f16 v[28:31], v[56:59], v[148:151], v[28:31]
	v_rcp_f32_e32 v243, v243
	v_mul_f32_e32 v247, v229, v229
	v_mul_f32_e32 v246, s90, v246
	v_mfma_f32_16x16x32_f16 v[24:27], v[64:67], v[148:151], v[24:27]
	v_mul_f32_e32 v247, s90, v247
	v_fma_f32 v244, v242, s82, v248
	v_mfma_f32_16x16x32_f16 v[12:15], v[56:59], v[156:159], v[12:15]
	v_fma_f32 v245, v243, s82, v248
	v_exp_f32_e32 v246, v246
	v_mfma_f32_16x16x32_f16 v[8:11], v[64:67], v[156:159], v[8:11]
	v_exp_f32_e32 v247, v247
	v_fmaak_f32 v244, v242, v244, 0x3f35f0e3
	v_fmaak_f32 v245, v243, v245, 0x3f35f0e3
	s_setprio 0
	s_barrier
	s_add_i32 s76, s68, s54
	v_lshl_add_u64 v[126:127], v[40:41], 0, s[44:45]
	s_mov_b32 m0, s76
	ds_read_b128 v[44:47], v130 offset:32768
	ds_read_b128 v[56:59], v130 offset:33792
	ds_read_b128 v[60:63], v130 offset:34816
	ds_read_b128 v[64:67], v130 offset:35840
	global_load_lds_dwordx4 v[126:127], off
	v_lshl_add_u64 v[126:127], v[42:43], 0, s[44:45]
	s_add_i32 m0, s76, 0x2000
	s_nop 0
	global_load_lds_dwordx4 v[126:127], off
	s_waitcnt vmcnt(7)
	s_barrier
	s_waitcnt lgkmcnt(0)
	s_setprio 1
	s_waitcnt lgkmcnt(0)
	v_mfma_f32_16x16x32_f16 v[84:87], v[44:47], v[68:71], v[84:87]
	v_fmaak_f32 v244, v242, v244, 0xbe11a98e
	v_fmaak_f32 v245, v243, v245, 0xbe11a98e
	v_mfma_f32_16x16x32_f16 v[52:55], v[44:47], v[136:139], v[52:55]
	v_fmaak_f32 v244, v242, v244, 0x3e027906
	v_fmaak_f32 v245, v243, v245, 0x3e027906
	v_mul_f32_e32 v244, v242, v244
	v_mfma_f32_16x16x32_f16 v[48:51], v[60:63], v[136:139], v[48:51]
	v_mul_f32_e32 v245, v243, v245
	v_max_f32_e32 v242, 0, v228
	v_mfma_f32_16x16x32_f16 v[20:23], v[44:47], v[144:147], v[20:23]
	v_max_f32_e32 v243, 0, v229
	v_mul_f32_e32 v244, v244, v246
	v_mfma_f32_16x16x32_f16 v[16:19], v[60:63], v[144:147], v[16:19]
	v_mul_f32_e32 v245, v245, v247
	v_fma_f32 v244, -|v228|, v244, v242
	v_fma_f32 v245, -|v229|, v245, v243
	v_mfma_f32_16x16x32_f16 v[4:7], v[44:47], v[152:155], v[4:7]
	v_cvt_pk_f16_f32 v226, v244, v245
	v_fma_f32 v242, |v230|, s80, 1.0
	v_mfma_f32_16x16x32_f16 v[0:3], v[60:63], v[152:155], v[0:3]
	v_fma_f32 v243, |v231|, s80, 1.0
	v_mul_f32_e32 v246, v230, v230
	v_rcp_f32_e32 v242, v242
	v_mfma_f32_16x16x32_f16 v[84:87], v[56:59], v[96:99], v[84:87]
	v_rcp_f32_e32 v243, v243
	v_mul_f32_e32 v247, v231, v231
	v_mfma_f32_16x16x32_f16 v[68:71], v[60:63], v[68:71], v[80:83]
	v_mul_f32_e32 v246, s90, v246
	v_mul_f32_e32 v247, s90, v247
	v_mfma_f32_16x16x32_f16 v[52:55], v[56:59], v[140:143], v[52:55]
	v_fma_f32 v244, v242, s82, v248
	v_fma_f32 v245, v243, s82, v248
	v_exp_f32_e32 v246, v246
	v_mfma_f32_16x16x32_f16 v[48:51], v[64:67], v[140:143], v[48:51]
	v_exp_f32_e32 v247, v247
	v_fmaak_f32 v244, v242, v244, 0x3f35f0e3
	v_mfma_f32_16x16x32_f16 v[20:23], v[56:59], v[148:151], v[20:23]
	v_fmaak_f32 v245, v243, v245, 0x3f35f0e3
	v_fmaak_f32 v244, v242, v244, 0xbe11a98e
	v_mfma_f32_16x16x32_f16 v[16:19], v[64:67], v[148:151], v[16:19]
	v_fmaak_f32 v245, v243, v245, 0xbe11a98e
	v_fmaak_f32 v244, v242, v244, 0x3e027906
	v_fmaak_f32 v245, v243, v245, 0x3e027906
	v_mfma_f32_16x16x32_f16 v[4:7], v[56:59], v[156:159], v[4:7]
	v_mul_f32_e32 v244, v242, v244
	v_mul_f32_e32 v245, v243, v245
	v_mfma_f32_16x16x32_f16 v[0:3], v[64:67], v[156:159], v[0:3]
	v_max_f32_e32 v242, 0, v230
	v_max_f32_e32 v243, 0, v231
	v_mul_f32_e32 v244, v244, v246
	v_mfma_f32_16x16x32_f16 v[68:71], v[64:67], v[96:99], v[68:71]
	v_mul_f32_e32 v245, v245, v247
	v_fma_f32 v244, -|v230|, v244, v242
	s_setprio 0
	s_barrier
	s_add_i32 s76, 0, 0x10000
	s_mov_b32 m0, s57
	v_add_u32_e32 v64, s76, v128
	v_lshl_add_u64 v[126:127], s[48:49], 0, v[100:101]
	ds_read_b128 v[44:47], v64
	ds_read_b128 v[56:59], v64 offset:1024
	ds_read_b128 v[60:63], v64 offset:2048
	ds_read_b128 v[64:67], v64 offset:3072
	ds_read_b128 v[80:83], v131 offset:49152
	ds_read_b128 v[96:99], v131 offset:50176
	ds_read_b128 v[136:139], v131 offset:51200
	ds_read_b128 v[140:143], v131 offset:52224
	ds_read_b128 v[144:147], v131 offset:53248
	ds_read_b128 v[148:151], v131 offset:54272
	ds_read_b128 v[152:155], v131 offset:55296
	ds_read_b128 v[156:159], v131 offset:56320
	global_load_lds_dwordx4 v[126:127], off
	v_lshl_add_u64 v[160:161], s[48:49], 0, v[104:105]
	s_mov_b32 m0, s58
	v_lshl_add_u64 v[162:163], s[46:47], 0, v[102:103]
	global_load_lds_dwordx4 v[160:161], off
	s_mov_b32 m0, s59
	v_lshl_add_u64 v[164:165], s[46:47], 0, v[106:107]
	global_load_lds_dwordx4 v[162:163], off
	s_mov_b32 m0, s60
	s_nop 0
	global_load_lds_dwordx4 v[164:165], off
	s_barrier
	s_waitcnt lgkmcnt(0)
	s_setprio 1
	s_waitcnt lgkmcnt(0)
	v_mfma_f32_16x16x32_f16 v[92:95], v[44:47], v[80:83], v[92:95]
	v_fma_f32 v245, -|v231|, v245, v243
	v_cvt_pk_f16_f32 v227, v244, v245
	v_mfma_f32_16x16x32_f16 v[88:91], v[60:63], v[80:83], v[88:91]
	v_lshl_add_u64 v[252:253], v[250:251], 0, s[96:97]
	global_store_dwordx4 v[252:253], v[224:227], off sc1
	v_fma_f32 v242, |v232|, s80, 1.0
	v_mfma_f32_16x16x32_f16 v[76:79], v[44:47], v[136:139], v[76:79]
	v_fma_f32 v243, |v233|, s80, 1.0
	v_mul_f32_e32 v246, v232, v232
	v_mfma_f32_16x16x32_f16 v[72:75], v[60:63], v[136:139], v[72:75]
	v_rcp_f32_e32 v242, v242
	v_rcp_f32_e32 v243, v243
	v_mul_f32_e32 v247, v233, v233
	v_mfma_f32_16x16x32_f16 v[28:31], v[44:47], v[144:147], v[28:31]
	v_mul_f32_e32 v246, s90, v246
	v_mul_f32_e32 v247, s90, v247
	v_mfma_f32_16x16x32_f16 v[24:27], v[60:63], v[144:147], v[24:27]
	v_fma_f32 v244, v242, s82, v248
	v_fma_f32 v245, v243, s82, v248
	v_mfma_f32_16x16x32_f16 v[12:15], v[44:47], v[152:155], v[12:15]
	v_exp_f32_e32 v246, v246
	v_exp_f32_e32 v247, v247
	v_fmaak_f32 v244, v242, v244, 0x3f35f0e3
	v_mfma_f32_16x16x32_f16 v[8:11], v[60:63], v[152:155], v[8:11]
	v_fmaak_f32 v245, v243, v245, 0x3f35f0e3
	v_fmaak_f32 v244, v242, v244, 0xbe11a98e
	v_mfma_f32_16x16x32_f16 v[92:95], v[56:59], v[96:99], v[92:95]
	v_fmaak_f32 v245, v243, v245, 0xbe11a98e
	v_fmaak_f32 v244, v242, v244, 0x3e027906
	v_mfma_f32_16x16x32_f16 v[88:91], v[64:67], v[96:99], v[88:91]
	v_fmaak_f32 v245, v243, v245, 0x3e027906
	v_mul_f32_e32 v244, v242, v244
	v_mul_f32_e32 v245, v243, v245
	v_mfma_f32_16x16x32_f16 v[76:79], v[56:59], v[140:143], v[76:79]
	v_max_f32_e32 v242, 0, v232
	v_max_f32_e32 v243, 0, v233
	v_mfma_f32_16x16x32_f16 v[72:75], v[64:67], v[140:143], v[72:75]
	v_mul_f32_e32 v244, v244, v246
	v_mul_f32_e32 v245, v245, v247
	v_fma_f32 v244, -|v232|, v244, v242
	v_mfma_f32_16x16x32_f16 v[28:31], v[56:59], v[148:151], v[28:31]
	v_fma_f32 v245, -|v233|, v245, v243
	v_cvt_pk_f16_f32 v232, v244, v245
	v_mfma_f32_16x16x32_f16 v[24:27], v[64:67], v[148:151], v[24:27]
	v_fma_f32 v242, |v234|, s80, 1.0
	v_fma_f32 v243, |v235|, s80, 1.0
	v_mfma_f32_16x16x32_f16 v[12:15], v[56:59], v[156:159], v[12:15]
	v_mul_f32_e32 v246, v234, v234
	v_rcp_f32_e32 v242, v242
	v_rcp_f32_e32 v243, v243
	v_mfma_f32_16x16x32_f16 v[8:11], v[64:67], v[156:159], v[8:11]
	v_mul_f32_e32 v247, v235, v235
	v_mul_f32_e32 v246, s90, v246
	s_setprio 0
	s_barrier
	s_add_i32 s48, 0, 0x14000
	s_add_u32 s46, s46, s10
	s_addc_u32 s47, s47, s11
	s_mov_b32 m0, s61
	v_add_u32_e32 v64, s48, v128
	v_lshl_add_u64 v[166:167], s[46:47], 0, v[102:103]
	ds_read_b128 v[44:47], v64
	ds_read_b128 v[56:59], v64 offset:1024
	ds_read_b128 v[60:63], v64 offset:2048
	ds_read_b128 v[64:67], v64 offset:3072
	global_load_lds_dwordx4 v[166:167], off
	v_lshl_add_u64 v[168:169], s[46:47], 0, v[106:107]
	s_mov_b32 m0, s62
	s_nop 0
	global_load_lds_dwordx4 v[168:169], off
	s_waitcnt vmcnt(7)
	s_barrier
	s_waitcnt lgkmcnt(0)
	s_setprio 1
	s_waitcnt lgkmcnt(0)
	v_mfma_f32_16x16x32_f16 v[84:87], v[44:47], v[80:83], v[84:87]
	v_mul_f32_e32 v247, s90, v247
	v_fma_f32 v244, v242, s82, v248
	v_fma_f32 v245, v243, s82, v248
	v_mfma_f32_16x16x32_f16 v[52:55], v[44:47], v[136:139], v[52:55]
	v_exp_f32_e32 v246, v246
	v_exp_f32_e32 v247, v247
	v_mfma_f32_16x16x32_f16 v[48:51], v[60:63], v[136:139], v[48:51]
	v_fmaak_f32 v244, v242, v244, 0x3f35f0e3
	v_fmaak_f32 v245, v243, v245, 0x3f35f0e3
	v_mfma_f32_16x16x32_f16 v[20:23], v[44:47], v[144:147], v[20:23]
	v_fmaak_f32 v244, v242, v244, 0xbe11a98e
	v_fmaak_f32 v245, v243, v245, 0xbe11a98e
	v_fmaak_f32 v244, v242, v244, 0x3e027906
	v_mfma_f32_16x16x32_f16 v[16:19], v[60:63], v[144:147], v[16:19]
	v_fmaak_f32 v245, v243, v245, 0x3e027906
	v_mul_f32_e32 v244, v242, v244
	v_mfma_f32_16x16x32_f16 v[4:7], v[44:47], v[152:155], v[4:7]
	v_mul_f32_e32 v245, v243, v245
	v_max_f32_e32 v242, 0, v234
	v_mfma_f32_16x16x32_f16 v[0:3], v[60:63], v[152:155], v[0:3]
	v_max_f32_e32 v243, 0, v235
	v_mul_f32_e32 v244, v244, v246
	v_mul_f32_e32 v245, v245, v247
	v_mfma_f32_16x16x32_f16 v[84:87], v[56:59], v[96:99], v[84:87]
	v_fma_f32 v244, -|v234|, v244, v242
	v_fma_f32 v245, -|v235|, v245, v243
	v_mfma_f32_16x16x32_f16 v[68:71], v[60:63], v[80:83], v[68:71]
	v_cvt_pk_f16_f32 v233, v244, v245
	v_fma_f32 v242, |v236|, s80, 1.0
	v_fma_f32 v243, |v237|, s80, 1.0
	v_mfma_f32_16x16x32_f16 v[52:55], v[56:59], v[140:143], v[52:55]
	v_mul_f32_e32 v246, v236, v236
	v_rcp_f32_e32 v242, v242
	v_mfma_f32_16x16x32_f16 v[48:51], v[64:67], v[140:143], v[48:51]
	v_rcp_f32_e32 v243, v243
	v_mul_f32_e32 v247, v237, v237
	v_mfma_f32_16x16x32_f16 v[20:23], v[56:59], v[148:151], v[20:23]
	v_mul_f32_e32 v246, s90, v246
	v_mul_f32_e32 v247, s90, v247
	v_fma_f32 v244, v242, s82, v248
	v_mfma_f32_16x16x32_f16 v[16:19], v[64:67], v[148:151], v[16:19]
	v_fma_f32 v245, v243, s82, v248
	v_exp_f32_e32 v246, v246
	v_mfma_f32_16x16x32_f16 v[4:7], v[56:59], v[156:159], v[4:7]
	v_exp_f32_e32 v247, v247
	v_fmaak_f32 v244, v242, v244, 0x3f35f0e3
	v_fmaak_f32 v245, v243, v245, 0x3f35f0e3
	v_mfma_f32_16x16x32_f16 v[0:3], v[64:67], v[156:159], v[0:3]
	v_fmaak_f32 v244, v242, v244, 0xbe11a98e
	v_fmaak_f32 v245, v243, v245, 0xbe11a98e
	v_mfma_f32_16x16x32_f16 v[68:71], v[64:67], v[96:99], v[68:71]
	v_fmaak_f32 v244, v242, v244, 0x3e027906
	v_fmaak_f32 v245, v243, v245, 0x3e027906
	s_setprio 0
	s_barrier
	s_mov_b32 m0, s64
	v_lshl_add_u64 v[126:127], v[126:127], 0, s[22:23]
	ds_read_b128 v[44:47], v132
	ds_read_b128 v[56:59], v132 offset:1024
	ds_read_b128 v[60:63], v132 offset:2048
	ds_read_b128 v[64:67], v132 offset:3072
	ds_read_b128 v[80:83], v133
	ds_read_b128 v[96:99], v133 offset:1024
	ds_read_b128 v[136:139], v133 offset:2048
	ds_read_b128 v[140:143], v133 offset:3072
	ds_read_b128 v[144:147], v133 offset:4096
	ds_read_b128 v[148:151], v133 offset:5120
	ds_read_b128 v[152:155], v133 offset:6144
	ds_read_b128 v[156:159], v133 offset:7168
	global_load_lds_dwordx4 v[126:127], off
	v_lshl_add_u64 v[126:127], v[160:161], 0, s[22:23]
	s_mov_b32 m0, s65
	s_add_i32 s46, s76, s54
	global_load_lds_dwordx4 v[126:127], off
	v_lshl_add_u64 v[126:127], v[162:163], 0, s[22:23]
	s_mov_b32 m0, s46
	s_nop 0
	global_load_lds_dwordx4 v[126:127], off
	v_lshl_add_u64 v[126:127], v[164:165], 0, s[22:23]
	s_add_i32 m0, s46, 0x2000
	s_nop 0
	global_load_lds_dwordx4 v[126:127], off
	s_barrier
	s_waitcnt lgkmcnt(0)
	s_setprio 1
	s_waitcnt lgkmcnt(0)
	v_mfma_f32_16x16x32_f16 v[92:95], v[44:47], v[80:83], v[92:95]
	v_mul_f32_e32 v244, v242, v244
	v_mul_f32_e32 v245, v243, v245
	v_max_f32_e32 v242, 0, v236
	v_mfma_f32_16x16x32_f16 v[88:91], v[60:63], v[80:83], v[88:91]
	v_max_f32_e32 v243, 0, v237
	v_mul_f32_e32 v244, v244, v246
	v_mfma_f32_16x16x32_f16 v[76:79], v[44:47], v[136:139], v[76:79]
	v_mul_f32_e32 v245, v245, v247
	v_fma_f32 v244, -|v236|, v244, v242
	v_mfma_f32_16x16x32_f16 v[72:75], v[60:63], v[136:139], v[72:75]
	v_fma_f32 v245, -|v237|, v245, v243
	v_cvt_pk_f16_f32 v234, v244, v245
	v_fma_f32 v242, |v238|, s80, 1.0
	v_mfma_f32_16x16x32_f16 v[28:31], v[44:47], v[144:147], v[28:31]
	v_fma_f32 v243, |v239|, s80, 1.0
	v_mul_f32_e32 v246, v238, v238
	v_mfma_f32_16x16x32_f16 v[24:27], v[60:63], v[144:147], v[24:27]
	v_rcp_f32_e32 v242, v242
	v_rcp_f32_e32 v243, v243
	v_mul_f32_e32 v247, v239, v239
	v_mfma_f32_16x16x32_f16 v[12:15], v[44:47], v[152:155], v[12:15]
	v_mul_f32_e32 v246, s90, v246
	v_mul_f32_e32 v247, s90, v247
	v_mfma_f32_16x16x32_f16 v[8:11], v[60:63], v[152:155], v[8:11]
	v_fma_f32 v244, v242, s82, v248
	v_fma_f32 v245, v243, s82, v248
	v_mfma_f32_16x16x32_f16 v[92:95], v[56:59], v[96:99], v[92:95]
	v_exp_f32_e32 v246, v246
	v_exp_f32_e32 v247, v247
	v_fmaak_f32 v244, v242, v244, 0x3f35f0e3
	v_mfma_f32_16x16x32_f16 v[88:91], v[64:67], v[96:99], v[88:91]
	v_fmaak_f32 v245, v243, v245, 0x3f35f0e3
	v_fmaak_f32 v244, v242, v244, 0xbe11a98e
	v_mfma_f32_16x16x32_f16 v[76:79], v[56:59], v[140:143], v[76:79]
	v_fmaak_f32 v245, v243, v245, 0xbe11a98e
	v_fmaak_f32 v244, v242, v244, 0x3e027906
	v_fmaak_f32 v245, v243, v245, 0x3e027906
	v_mfma_f32_16x16x32_f16 v[72:75], v[64:67], v[140:143], v[72:75]
	v_mul_f32_e32 v244, v242, v244
	v_mul_f32_e32 v245, v243, v245
	v_mfma_f32_16x16x32_f16 v[28:31], v[56:59], v[148:151], v[28:31]
	v_max_f32_e32 v242, 0, v238
	v_max_f32_e32 v243, 0, v239
	v_mfma_f32_16x16x32_f16 v[24:27], v[64:67], v[148:151], v[24:27]
	v_mul_f32_e32 v244, v244, v246
	v_mul_f32_e32 v245, v245, v247
	v_fma_f32 v244, -|v238|, v244, v242
	v_mfma_f32_16x16x32_f16 v[12:15], v[56:59], v[156:159], v[12:15]
	v_fma_f32 v245, -|v239|, v245, v243
	v_cvt_pk_f16_f32 v235, v244, v245
	v_mfma_f32_16x16x32_f16 v[8:11], v[64:67], v[156:159], v[8:11]
	v_lshl_add_u64 v[252:253], v[250:251], 0, s[96:97]
	global_store_dwordx4 v[252:253], v[232:235], off offset:256 sc1
	s_setprio 0
	s_barrier
	s_add_i32 s46, s48, s54
	v_lshl_add_u64 v[126:127], v[166:167], 0, s[22:23]
	s_mov_b32 m0, s46
	ds_read_b128 v[44:47], v134
	ds_read_b128 v[56:59], v134 offset:1024
	ds_read_b128 v[60:63], v134 offset:2048
	ds_read_b128 v[64:67], v134 offset:3072
	global_load_lds_dwordx4 v[126:127], off
	v_lshl_add_u64 v[126:127], v[168:169], 0, s[22:23]
	s_add_i32 m0, s46, 0x2000
	s_nop 0
	global_load_lds_dwordx4 v[126:127], off
	s_waitcnt vmcnt(7)
	s_barrier
	s_waitcnt lgkmcnt(0)
	s_setprio 1
	s_waitcnt lgkmcnt(0)
	v_mfma_f32_16x16x32_f16 v[84:87], v[44:47], v[80:83], v[84:87]
	v_mfma_f32_16x16x32_f16 v[68:71], v[60:63], v[80:83], v[68:71]
	v_mfma_f32_16x16x32_f16 v[52:55], v[44:47], v[136:139], v[52:55]
	v_mfma_f32_16x16x32_f16 v[48:51], v[60:63], v[136:139], v[48:51]
	v_mfma_f32_16x16x32_f16 v[20:23], v[44:47], v[144:147], v[20:23]
	v_mfma_f32_16x16x32_f16 v[16:19], v[60:63], v[144:147], v[16:19]
	v_mfma_f32_16x16x32_f16 v[4:7], v[44:47], v[152:155], v[4:7]
	v_mfma_f32_16x16x32_f16 v[0:3], v[60:63], v[152:155], v[0:3]
	v_mfma_f32_16x16x32_f16 v[84:87], v[56:59], v[96:99], v[84:87]
	v_mfma_f32_16x16x32_f16 v[80:83], v[64:67], v[96:99], v[68:71]
	v_mfma_f32_16x16x32_f16 v[52:55], v[56:59], v[140:143], v[52:55]
	v_mfma_f32_16x16x32_f16 v[48:51], v[64:67], v[140:143], v[48:51]
	v_mfma_f32_16x16x32_f16 v[20:23], v[56:59], v[148:151], v[20:23]
	v_mfma_f32_16x16x32_f16 v[16:19], v[64:67], v[148:151], v[16:19]
	v_mfma_f32_16x16x32_f16 v[4:7], v[56:59], v[156:159], v[4:7]
	v_mfma_f32_16x16x32_f16 v[0:3], v[64:67], v[156:159], v[0:3]
	s_setprio 0
	s_barrier
	s_add_i32 s75, s75, 3
	s_add_u32 s44, s44, 0x180
	s_addc_u32 s45, s45, 0
	s_branch .LBB5_42
